# swiglu epilogues: the dead v_mov 0 before each pair of v_cvt_pk_fp8_f32 (low half, then op_sel high half) removed - 16 VALU issues fewer per unit
# speedup vs baseline: 1.0032x; 1.0032x over previous
.LBB0_1197:
	v_cvt_f32_i32_e32 v129, v129
	v_cvt_f32_i32_e32 v128, v128
	v_pk_mul_f32 v[130:131], v[204:205], v[220:221] op_sel_hi:[1,0]
	v_cvt_f32_i32_e32 v127, v127
	v_mul_f32_e32 v132, 0xbfb8aa3b, v130
	v_pk_mul_f32 v[136:137], v[128:129], v[132:133] op_sel_hi:[1,0]
	v_cvt_f32_i32_e32 v126, v126
	v_cvt_f32_i32_e32 v123, v123
	v_cvt_f32_i32_e32 v122, v122
	v_cvt_f32_i32_e32 v119, v119
	v_cvt_f32_i32_e32 v118, v118
	v_cvt_f32_i32_e32 v121, v121
	v_cvt_f32_i32_e32 v120, v120
	v_exp_f32_e32 v136, v136
	v_exp_f32_e32 v137, v137
	v_pk_mul_f32 v[134:135], v[126:127], v[132:133] op_sel_hi:[1,0]
	v_pk_mul_f32 v[120:121], v[120:121], v[128:129]
	v_pk_mul_f32 v[118:119], v[118:119], v[126:127]
	v_pk_add_f32 v[126:127], v[136:137], 1.0 op_sel_hi:[1,0]
	v_pk_mul_f32 v[128:129], v[122:123], v[132:133] op_sel_hi:[1,0]
	v_cvt_f32_i32_e32 v125, v125
	v_cvt_f32_i32_e32 v124, v124
	v_exp_f32_e32 v134, v134
	v_exp_f32_e32 v135, v135
	v_rcp_f32_e32 v126, v126
	v_rcp_f32_e32 v127, v127
	v_exp_f32_e32 v128, v128
	v_exp_f32_e32 v129, v129
	v_mul_f32_e32 v130, v130, v131
	v_mul_f32_e32 v130, 0x41000000, v130
	v_pk_mul_f32 v[120:121], v[120:121], v[130:131] op_sel_hi:[1,0]
	v_cvt_f32_i32_e32 v115, v115
	v_cvt_f32_i32_e32 v114, v114
	v_pk_add_f32 v[134:135], v[134:135], 1.0 op_sel_hi:[1,0]
	v_pk_mul_f32 v[120:121], v[120:121], v[126:127]
	v_pk_add_f32 v[126:127], v[128:129], 1.0 op_sel_hi:[1,0]
	v_pk_mul_f32 v[128:129], v[124:125], v[132:133] op_sel_hi:[1,0]
	v_cvt_f32_i32_e32 v117, v117
	v_cvt_f32_i32_e32 v116, v116
	v_rcp_f32_e32 v134, v134
	v_rcp_f32_e32 v135, v135
	v_exp_f32_e32 v128, v128
	v_exp_f32_e32 v129, v129
	v_rcp_f32_e32 v126, v126
	v_rcp_f32_e32 v127, v127
	v_pk_mul_f32 v[118:119], v[118:119], v[130:131] op_sel_hi:[1,0]
	v_pk_mul_f32 v[114:115], v[114:115], v[122:123]
	v_pk_mul_f32 v[118:119], v[118:119], v[134:135]
	v_pk_mul_f32 v[116:117], v[116:117], v[124:125]
	v_pk_add_f32 v[122:123], v[128:129], 1.0 op_sel_hi:[1,0]
	v_pk_mul_f32 v[114:115], v[114:115], v[130:131] op_sel_hi:[1,0]
	v_rcp_f32_e32 v122, v122
	v_rcp_f32_e32 v123, v123
	v_pk_mul_f32 v[124:125], v[114:115], v[126:127]
	v_pk_mul_f32 v[114:115], v[116:117], v[130:131] op_sel_hi:[1,0]
	v_med3_f32 v117, v118, s54, v221
	v_med3_f32 v118, v119, s54, v221
	v_cvt_pk_fp8_f32 v116, v117, v118
	v_med3_f32 v118, v120, s54, v221
	v_med3_f32 v119, v121, s54, v221
	v_med3_f32 v120, v124, s54, v221
	v_med3_f32 v121, v125, s54, v221
	v_cvt_pk_fp8_f32 v117, v120, v121
	v_pk_mul_f32 v[122:123], v[114:115], v[122:123]
	v_cvt_f32_i32_e32 v113, v113
	v_cvt_f32_i32_e32 v112, v112
	v_cvt_pk_fp8_f32 v116, v118, v119 op_sel:[0,0,1]
	v_med3_f32 v118, v122, s54, v221
	v_med3_f32 v119, v123, s54, v221
	v_cvt_pk_fp8_f32 v117, v118, v119 op_sel:[0,0,1]
	v_pk_mul_f32 v[118:119], v[204:205], v[218:219] op_sel_hi:[1,0]
	v_cvt_f32_i32_e32 v111, v111
	v_mul_f32_e32 v120, 0xbfb8aa3b, v118
	v_pk_mul_f32 v[124:125], v[112:113], v[120:121] op_sel_hi:[1,0]
	v_cvt_f32_i32_e32 v110, v110
	v_cvt_f32_i32_e32 v107, v107
	v_cvt_f32_i32_e32 v106, v106
	v_cvt_f32_i32_e32 v103, v103
	v_cvt_f32_i32_e32 v102, v102
	v_cvt_f32_i32_e32 v105, v105
	v_cvt_f32_i32_e32 v104, v104
	v_exp_f32_e32 v124, v124
	v_exp_f32_e32 v125, v125
	v_pk_mul_f32 v[122:123], v[110:111], v[120:121] op_sel_hi:[1,0]
	v_pk_mul_f32 v[104:105], v[104:105], v[112:113]
	v_pk_mul_f32 v[102:103], v[102:103], v[110:111]
	v_pk_add_f32 v[110:111], v[124:125], 1.0 op_sel_hi:[1,0]
	v_pk_mul_f32 v[112:113], v[106:107], v[120:121] op_sel_hi:[1,0]
	v_cvt_f32_i32_e32 v109, v109
	v_cvt_f32_i32_e32 v108, v108
	v_rcp_f32_e32 v110, v110
	v_rcp_f32_e32 v111, v111
	v_exp_f32_e32 v112, v112
	v_exp_f32_e32 v113, v113
	v_mul_f32_e32 v118, v118, v119
	v_mul_f32_e32 v118, 0x41000000, v118
	v_pk_mul_f32 v[104:105], v[104:105], v[118:119] op_sel_hi:[1,0]
	v_exp_f32_e32 v122, v122
	v_exp_f32_e32 v123, v123
	v_pk_mul_f32 v[104:105], v[104:105], v[110:111]
	v_pk_add_f32 v[110:111], v[112:113], 1.0 op_sel_hi:[1,0]
	v_pk_mul_f32 v[112:113], v[108:109], v[120:121] op_sel_hi:[1,0]
	v_cvt_f32_i32_e32 v99, v99
	v_cvt_f32_i32_e32 v98, v98
	v_exp_f32_e32 v112, v112
	v_exp_f32_e32 v113, v113
	v_cvt_f32_i32_e32 v101, v101
	v_cvt_f32_i32_e32 v100, v100
	v_pk_add_f32 v[122:123], v[122:123], 1.0 op_sel_hi:[1,0]
	v_rcp_f32_e32 v110, v110
	v_rcp_f32_e32 v122, v122
	v_rcp_f32_e32 v123, v123
	v_rcp_f32_e32 v111, v111
	v_pk_mul_f32 v[98:99], v[98:99], v[106:107]
	v_pk_add_f32 v[106:107], v[112:113], 1.0 op_sel_hi:[1,0]
	v_pk_mul_f32 v[102:103], v[102:103], v[118:119] op_sel_hi:[1,0]
	v_rcp_f32_e32 v106, v106
	v_rcp_f32_e32 v107, v107
	v_pk_mul_f32 v[100:101], v[100:101], v[108:109]
	v_pk_mul_f32 v[98:99], v[98:99], v[118:119] op_sel_hi:[1,0]
	v_pk_mul_f32 v[102:103], v[102:103], v[122:123]
	v_pk_mul_f32 v[108:109], v[98:99], v[110:111]
	v_pk_mul_f32 v[98:99], v[100:101], v[118:119] op_sel_hi:[1,0]
	v_cvt_f32_i32_e32 v97, v97
	v_pk_mul_f32 v[100:101], v[98:99], v[106:107]
	v_med3_f32 v99, v102, s54, v221
	v_med3_f32 v102, v103, s54, v221
	v_cvt_pk_fp8_f32 v98, v99, v102
	v_med3_f32 v102, v104, s54, v221
	v_med3_f32 v103, v105, s54, v221
	v_med3_f32 v104, v108, s54, v221
	v_med3_f32 v105, v109, s54, v221
	v_cvt_pk_fp8_f32 v99, v104, v105
	v_cvt_f32_i32_e32 v96, v96
	v_med3_f32 v100, v100, s54, v221
	v_med3_f32 v101, v101, s54, v221
	v_cvt_pk_fp8_f32 v99, v100, v101 op_sel:[0,0,1]
	v_pk_mul_f32 v[100:101], v[204:205], v[216:217] op_sel_hi:[1,0]
	v_cvt_pk_fp8_f32 v98, v102, v103 op_sel:[0,0,1]
	v_mul_f32_e32 v102, 0xbfb8aa3b, v100
	v_pk_mul_f32 v[106:107], v[96:97], v[102:103] op_sel_hi:[1,0]
	v_cvt_f32_i32_e32 v95, v95
	v_cvt_f32_i32_e32 v94, v94
	v_cvt_f32_i32_e32 v91, v91
	v_cvt_f32_i32_e32 v90, v90
	v_cvt_f32_i32_e32 v87, v87
	v_cvt_f32_i32_e32 v86, v86
	v_cvt_f32_i32_e32 v89, v89
	v_cvt_f32_i32_e32 v88, v88
	v_exp_f32_e32 v106, v106
	v_exp_f32_e32 v107, v107
	v_pk_mul_f32 v[104:105], v[94:95], v[102:103] op_sel_hi:[1,0]
	v_pk_mul_f32 v[88:89], v[88:89], v[96:97]
	v_pk_mul_f32 v[86:87], v[86:87], v[94:95]
	v_pk_add_f32 v[94:95], v[106:107], 1.0 op_sel_hi:[1,0]
	v_pk_mul_f32 v[96:97], v[90:91], v[102:103] op_sel_hi:[1,0]
	v_cvt_f32_i32_e32 v93, v93
	v_cvt_f32_i32_e32 v92, v92
	v_rcp_f32_e32 v94, v94
	v_rcp_f32_e32 v95, v95
	v_exp_f32_e32 v96, v96
	v_exp_f32_e32 v97, v97
	v_mul_f32_e32 v100, v100, v101
	v_mul_f32_e32 v100, 0x41000000, v100
	v_pk_mul_f32 v[88:89], v[88:89], v[100:101] op_sel_hi:[1,0]
	v_exp_f32_e32 v104, v104
	v_exp_f32_e32 v105, v105
	v_pk_mul_f32 v[88:89], v[88:89], v[94:95]
	v_pk_add_f32 v[94:95], v[96:97], 1.0 op_sel_hi:[1,0]
	v_pk_mul_f32 v[96:97], v[92:93], v[102:103] op_sel_hi:[1,0]
	v_cvt_f32_i32_e32 v83, v83
	v_cvt_f32_i32_e32 v82, v82
	v_exp_f32_e32 v96, v96
	v_exp_f32_e32 v97, v97
	v_cvt_f32_i32_e32 v85, v85
	v_cvt_f32_i32_e32 v84, v84
	v_pk_add_f32 v[104:105], v[104:105], 1.0 op_sel_hi:[1,0]
	v_pk_mul_f32 v[82:83], v[82:83], v[90:91]
	v_rcp_f32_e32 v104, v104
	v_rcp_f32_e32 v105, v105
	v_pk_add_f32 v[90:91], v[96:97], 1.0 op_sel_hi:[1,0]
	v_rcp_f32_e32 v94, v94
	v_rcp_f32_e32 v95, v95
	v_rcp_f32_e32 v90, v90
	v_rcp_f32_e32 v91, v91
	v_pk_mul_f32 v[86:87], v[86:87], v[100:101] op_sel_hi:[1,0]
	v_pk_mul_f32 v[84:85], v[84:85], v[92:93]
	v_pk_mul_f32 v[86:87], v[86:87], v[104:105]
	v_pk_mul_f32 v[82:83], v[82:83], v[100:101] op_sel_hi:[1,0]
	v_pk_mul_f32 v[84:85], v[84:85], v[100:101] op_sel_hi:[1,0]
	v_pk_mul_f32 v[82:83], v[82:83], v[94:95]
	v_pk_mul_f32 v[84:85], v[84:85], v[90:91]
	v_med3_f32 v90, v86, s54, v221
	v_med3_f32 v87, v87, s54, v221
	v_cvt_pk_fp8_f32 v86, v90, v87
	v_med3_f32 v82, v82, s54, v221
	v_med3_f32 v83, v83, s54, v221
	v_cvt_pk_fp8_f32 v87, v82, v83
	v_cvt_f32_i32_e32 v81, v81
	v_cvt_f32_i32_e32 v80, v80
	v_med3_f32 v82, v84, s54, v221
	v_med3_f32 v83, v85, s54, v221
	v_cvt_pk_fp8_f32 v87, v82, v83 op_sel:[0,0,1]
	v_pk_mul_f32 v[82:83], v[204:205], v[214:215] op_sel_hi:[1,0]
	v_cvt_f32_i32_e32 v79, v79
	v_mul_f32_e32 v84, 0xbfb8aa3b, v82
	v_pk_mul_f32 v[90:91], v[80:81], v[84:85] op_sel_hi:[1,0]
	v_cvt_f32_i32_e32 v78, v78
	v_cvt_f32_i32_e32 v75, v75
	v_cvt_f32_i32_e32 v74, v74
	v_cvt_f32_i32_e32 v71, v71
	v_cvt_f32_i32_e32 v70, v70
	v_cvt_f32_i32_e32 v73, v73
	v_cvt_f32_i32_e32 v72, v72
	v_exp_f32_e32 v90, v90
	v_exp_f32_e32 v91, v91
	v_med3_f32 v88, v88, s54, v221
	v_med3_f32 v89, v89, s54, v221
	v_cvt_pk_fp8_f32 v86, v88, v89 op_sel:[0,0,1]
	v_pk_mul_f32 v[88:89], v[78:79], v[84:85] op_sel_hi:[1,0]
	v_pk_mul_f32 v[72:73], v[72:73], v[80:81]
	v_pk_mul_f32 v[70:71], v[70:71], v[78:79]
	v_pk_add_f32 v[78:79], v[90:91], 1.0 op_sel_hi:[1,0]
	v_pk_mul_f32 v[80:81], v[74:75], v[84:85] op_sel_hi:[1,0]
	v_cvt_f32_i32_e32 v77, v77
	v_cvt_f32_i32_e32 v76, v76
	v_rcp_f32_e32 v78, v78
	v_rcp_f32_e32 v79, v79
	v_exp_f32_e32 v80, v80
	v_exp_f32_e32 v81, v81
	v_mul_f32_e32 v82, v82, v83
	v_mul_f32_e32 v82, 0x41000000, v82
	v_pk_mul_f32 v[72:73], v[72:73], v[82:83] op_sel_hi:[1,0]
	v_exp_f32_e32 v88, v88
	v_exp_f32_e32 v89, v89
	v_pk_mul_f32 v[72:73], v[72:73], v[78:79]
	v_pk_add_f32 v[78:79], v[80:81], 1.0 op_sel_hi:[1,0]
	v_pk_mul_f32 v[80:81], v[76:77], v[84:85] op_sel_hi:[1,0]
	v_cvt_f32_i32_e32 v67, v67
	v_cvt_f32_i32_e32 v66, v66
	v_exp_f32_e32 v80, v80
	v_exp_f32_e32 v81, v81
	v_cvt_f32_i32_e32 v69, v69
	v_cvt_f32_i32_e32 v68, v68
	v_pk_add_f32 v[88:89], v[88:89], 1.0 op_sel_hi:[1,0]
	v_pk_mul_f32 v[66:67], v[66:67], v[74:75]
	v_rcp_f32_e32 v88, v88
	v_rcp_f32_e32 v89, v89
	v_pk_add_f32 v[74:75], v[80:81], 1.0 op_sel_hi:[1,0]
	v_rcp_f32_e32 v78, v78
	v_rcp_f32_e32 v79, v79
	v_rcp_f32_e32 v74, v74
	v_rcp_f32_e32 v75, v75
	v_pk_mul_f32 v[70:71], v[70:71], v[82:83] op_sel_hi:[1,0]
	v_pk_mul_f32 v[68:69], v[68:69], v[76:77]
	v_pk_mul_f32 v[70:71], v[70:71], v[88:89]
	v_pk_mul_f32 v[66:67], v[66:67], v[82:83] op_sel_hi:[1,0]
	v_pk_mul_f32 v[68:69], v[68:69], v[82:83] op_sel_hi:[1,0]
	v_pk_mul_f32 v[66:67], v[66:67], v[78:79]
	v_pk_mul_f32 v[68:69], v[68:69], v[74:75]
	v_med3_f32 v74, v70, s54, v221
	v_med3_f32 v71, v71, s54, v221
	v_cvt_pk_fp8_f32 v70, v74, v71
	v_med3_f32 v66, v66, s54, v221
	v_med3_f32 v67, v67, s54, v221
	v_cvt_pk_fp8_f32 v71, v66, v67
	s_lshl_b32 s9, s19, 2
	s_or_b32 s20, s9, s48
	v_cvt_f32_i32_e32 v65, v65
	v_cvt_f32_i32_e32 v64, v64
	s_ashr_i32 s21, s20, 31
	v_med3_f32 v66, v68, s54, v221
	v_med3_f32 v67, v69, s54, v221
	s_lshl_b64 s[20:21], s[20:21], 13
	s_mul_i32 s11, s18, 0x160000
	v_cvt_pk_fp8_f32 v71, v66, v67 op_sel:[0,0,1]
	v_pk_mul_f32 v[66:67], v[204:205], v[212:213] op_sel_hi:[1,0]
	s_mul_hi_i32 s9, s18, 0x160000
	s_add_u32 s11, s33, s11
	v_med3_f32 v72, v72, s54, v221
	v_med3_f32 v73, v73, s54, v221
	v_mul_f32_e32 v68, 0xbfb8aa3b, v66
	s_addc_u32 s9, s42, s9
	v_cvt_pk_fp8_f32 v70, v72, v73 op_sel:[0,0,1]
	v_pk_mul_f32 v[72:73], v[64:65], v[68:69] op_sel_hi:[1,0]
	s_add_u32 s18, s11, s20
	v_cvt_f32_i32_e32 v63, v63
	v_cvt_f32_i32_e32 v62, v62
	v_cvt_f32_i32_e32 v59, v59
	v_cvt_f32_i32_e32 v58, v58
	v_cvt_f32_i32_e32 v55, v55
	v_cvt_f32_i32_e32 v54, v54
	v_cvt_f32_i32_e32 v57, v57
	v_cvt_f32_i32_e32 v56, v56
	v_exp_f32_e32 v72, v72
	v_exp_f32_e32 v73, v73
	s_addc_u32 s19, s9, s21
	v_lshl_add_u64 v[114:115], s[18:19], 0, v[222:223]
	v_lshl_add_u64 v[114:115], v[114:115], 0, v[194:195]
	global_store_dwordx2 v[114:115], v[116:117], off
	global_store_dwordx2 v[114:115], v[98:99], off offset:512
	global_store_dwordx2 v[114:115], v[86:87], off offset:1024
	global_store_dwordx2 v[114:115], v[70:71], off offset:1536
	v_pk_mul_f32 v[70:71], v[62:63], v[68:69] op_sel_hi:[1,0]
	v_pk_mul_f32 v[56:57], v[56:57], v[64:65]
	v_pk_mul_f32 v[54:55], v[54:55], v[62:63]
	v_pk_add_f32 v[62:63], v[72:73], 1.0 op_sel_hi:[1,0]
	v_pk_mul_f32 v[64:65], v[58:59], v[68:69] op_sel_hi:[1,0]
	v_cvt_f32_i32_e32 v61, v61
	v_cvt_f32_i32_e32 v60, v60
	v_exp_f32_e32 v70, v70
	v_exp_f32_e32 v71, v71
	v_rcp_f32_e32 v62, v62
	v_rcp_f32_e32 v63, v63
	v_exp_f32_e32 v64, v64
	v_exp_f32_e32 v65, v65
	v_mul_f32_e32 v66, v66, v67
	v_mul_f32_e32 v66, 0x41000000, v66
	v_pk_mul_f32 v[56:57], v[56:57], v[66:67] op_sel_hi:[1,0]
	v_cvt_f32_i32_e32 v51, v51
	v_cvt_f32_i32_e32 v50, v50
	v_pk_add_f32 v[70:71], v[70:71], 1.0 op_sel_hi:[1,0]
	v_pk_mul_f32 v[56:57], v[56:57], v[62:63]
	v_pk_add_f32 v[62:63], v[64:65], 1.0 op_sel_hi:[1,0]
	v_pk_mul_f32 v[64:65], v[60:61], v[68:69] op_sel_hi:[1,0]
	v_rcp_f32_e32 v70, v70
	v_rcp_f32_e32 v71, v71
	v_exp_f32_e32 v64, v64
	v_exp_f32_e32 v65, v65
	v_cvt_f32_i32_e32 v53, v53
	v_cvt_f32_i32_e32 v52, v52
	v_rcp_f32_e32 v62, v62
	v_rcp_f32_e32 v63, v63
	v_pk_mul_f32 v[54:55], v[54:55], v[66:67] op_sel_hi:[1,0]
	v_pk_mul_f32 v[50:51], v[50:51], v[58:59]
	v_pk_mul_f32 v[54:55], v[54:55], v[70:71]
	v_pk_add_f32 v[58:59], v[64:65], 1.0 op_sel_hi:[1,0]
	v_pk_mul_f32 v[50:51], v[50:51], v[66:67] op_sel_hi:[1,0]
	v_pk_mul_f32 v[52:53], v[52:53], v[60:61]
	v_rcp_f32_e32 v58, v58
	v_rcp_f32_e32 v59, v59
	v_pk_mul_f32 v[50:51], v[50:51], v[62:63]
	v_med3_f32 v60, v54, s54, v221
	v_med3_f32 v55, v55, s54, v221
	v_cvt_pk_fp8_f32 v54, v60, v55
	v_med3_f32 v50, v50, s54, v221
	v_med3_f32 v51, v51, s54, v221
	v_cvt_pk_fp8_f32 v55, v50, v51
	v_pk_mul_f32 v[52:53], v[52:53], v[66:67] op_sel_hi:[1,0]
	v_cvt_f32_i32_e32 v49, v49
	v_pk_mul_f32 v[52:53], v[52:53], v[58:59]
	v_cvt_f32_i32_e32 v48, v48
	v_med3_f32 v50, v52, s54, v221
	v_med3_f32 v51, v53, s54, v221
	v_cvt_pk_fp8_f32 v55, v50, v51 op_sel:[0,0,1]
	v_pk_mul_f32 v[50:51], v[204:205], v[210:211] op_sel_hi:[1,0]
	v_cvt_f32_i32_e32 v47, v47
	v_mul_f32_e32 v52, 0xbfb8aa3b, v50
	v_pk_mul_f32 v[60:61], v[48:49], v[52:53] op_sel_hi:[1,0]
	v_cvt_f32_i32_e32 v46, v46
	v_cvt_f32_i32_e32 v43, v43
	v_cvt_f32_i32_e32 v42, v42
	v_cvt_f32_i32_e32 v39, v39
	v_cvt_f32_i32_e32 v38, v38
	v_cvt_f32_i32_e32 v41, v41
	v_cvt_f32_i32_e32 v40, v40
	v_exp_f32_e32 v60, v60
	v_exp_f32_e32 v61, v61
	v_med3_f32 v56, v56, s54, v221
	v_med3_f32 v57, v57, s54, v221
	v_cvt_pk_fp8_f32 v54, v56, v57 op_sel:[0,0,1]
	v_pk_mul_f32 v[56:57], v[46:47], v[52:53] op_sel_hi:[1,0]
	v_pk_mul_f32 v[40:41], v[40:41], v[48:49]
	v_pk_mul_f32 v[38:39], v[38:39], v[46:47]
	v_pk_add_f32 v[46:47], v[60:61], 1.0 op_sel_hi:[1,0]
	v_pk_mul_f32 v[48:49], v[42:43], v[52:53] op_sel_hi:[1,0]
	v_cvt_f32_i32_e32 v45, v45
	v_cvt_f32_i32_e32 v44, v44
	v_rcp_f32_e32 v46, v46
	v_rcp_f32_e32 v47, v47
	v_exp_f32_e32 v48, v48
	v_exp_f32_e32 v49, v49
	v_mul_f32_e32 v50, v50, v51
	v_mul_f32_e32 v50, 0x41000000, v50
	v_pk_mul_f32 v[40:41], v[40:41], v[50:51] op_sel_hi:[1,0]
	v_exp_f32_e32 v56, v56
	v_exp_f32_e32 v57, v57
	v_pk_mul_f32 v[40:41], v[40:41], v[46:47]
	v_pk_add_f32 v[46:47], v[48:49], 1.0 op_sel_hi:[1,0]
	v_pk_mul_f32 v[48:49], v[44:45], v[52:53] op_sel_hi:[1,0]
	v_cvt_f32_i32_e32 v35, v35
	v_cvt_f32_i32_e32 v34, v34
	v_exp_f32_e32 v48, v48
	v_exp_f32_e32 v49, v49
	v_cvt_f32_i32_e32 v37, v37
	v_cvt_f32_i32_e32 v36, v36
	v_pk_add_f32 v[56:57], v[56:57], 1.0 op_sel_hi:[1,0]
	v_pk_mul_f32 v[34:35], v[34:35], v[42:43]
	v_rcp_f32_e32 v56, v56
	v_rcp_f32_e32 v57, v57
	v_pk_add_f32 v[42:43], v[48:49], 1.0 op_sel_hi:[1,0]
	v_rcp_f32_e32 v46, v46
	v_rcp_f32_e32 v47, v47
	v_rcp_f32_e32 v42, v42
	v_rcp_f32_e32 v43, v43
	v_pk_mul_f32 v[38:39], v[38:39], v[50:51] op_sel_hi:[1,0]
	v_pk_mul_f32 v[36:37], v[36:37], v[44:45]
	v_pk_mul_f32 v[38:39], v[38:39], v[56:57]
	v_pk_mul_f32 v[34:35], v[34:35], v[50:51] op_sel_hi:[1,0]
	v_pk_mul_f32 v[36:37], v[36:37], v[50:51] op_sel_hi:[1,0]
	v_pk_mul_f32 v[34:35], v[34:35], v[46:47]
	v_pk_mul_f32 v[36:37], v[36:37], v[42:43]
	v_med3_f32 v42, v38, s54, v221
	v_med3_f32 v39, v39, s54, v221
	v_cvt_pk_fp8_f32 v38, v42, v39
	v_med3_f32 v34, v34, s54, v221
	v_med3_f32 v35, v35, s54, v221
	v_cvt_pk_fp8_f32 v39, v34, v35
	v_med3_f32 v40, v40, s54, v221
	v_med3_f32 v41, v41, s54, v221
	v_med3_f32 v34, v36, s54, v221
	v_med3_f32 v35, v37, s54, v221
	v_cvt_pk_fp8_f32 v38, v40, v41 op_sel:[0,0,1]
	v_cvt_pk_fp8_f32 v39, v34, v35 op_sel:[0,0,1]
	v_lshl_add_u64 v[34:35], s[18:19], 0, v[226:227]
	v_cvt_f32_i32_e32 v33, v33
	v_cvt_f32_i32_e32 v32, v32
	v_lshl_add_u64 v[34:35], v[34:35], 0, v[194:195]
	global_store_dwordx2 v[34:35], v[38:39], off
	v_pk_mul_f32 v[34:35], v[204:205], v[208:209] op_sel_hi:[1,0]
	v_cvt_f32_i32_e32 v31, v31
	v_mul_f32_e32 v36, 0xbfb8aa3b, v34
	v_pk_mul_f32 v[40:41], v[32:33], v[36:37] op_sel_hi:[1,0]
	v_cvt_f32_i32_e32 v30, v30
	v_cvt_f32_i32_e32 v27, v27
	v_cvt_f32_i32_e32 v26, v26
	v_cvt_f32_i32_e32 v23, v23
	v_cvt_f32_i32_e32 v22, v22
	v_cvt_f32_i32_e32 v25, v25
	v_cvt_f32_i32_e32 v24, v24
	v_exp_f32_e32 v40, v40
	v_exp_f32_e32 v41, v41
	v_pk_mul_f32 v[38:39], v[30:31], v[36:37] op_sel_hi:[1,0]
	v_pk_mul_f32 v[24:25], v[24:25], v[32:33]
	v_pk_mul_f32 v[22:23], v[22:23], v[30:31]
	v_pk_add_f32 v[30:31], v[40:41], 1.0 op_sel_hi:[1,0]
	v_pk_mul_f32 v[32:33], v[26:27], v[36:37] op_sel_hi:[1,0]
	v_cvt_f32_i32_e32 v29, v29
	v_cvt_f32_i32_e32 v28, v28
	v_exp_f32_e32 v38, v38
	v_exp_f32_e32 v39, v39
	v_rcp_f32_e32 v30, v30
	v_rcp_f32_e32 v31, v31
	v_exp_f32_e32 v32, v32
	v_exp_f32_e32 v33, v33
	v_mul_f32_e32 v34, v34, v35
	v_mul_f32_e32 v34, 0x41000000, v34
	v_pk_mul_f32 v[24:25], v[24:25], v[34:35] op_sel_hi:[1,0]
	v_cvt_f32_i32_e32 v19, v19
	v_cvt_f32_i32_e32 v18, v18
	v_pk_add_f32 v[38:39], v[38:39], 1.0 op_sel_hi:[1,0]
	v_pk_mul_f32 v[24:25], v[24:25], v[30:31]
	v_pk_add_f32 v[30:31], v[32:33], 1.0 op_sel_hi:[1,0]
	v_pk_mul_f32 v[32:33], v[28:29], v[36:37] op_sel_hi:[1,0]
	v_rcp_f32_e32 v38, v38
	v_rcp_f32_e32 v39, v39
	v_exp_f32_e32 v32, v32
	v_exp_f32_e32 v33, v33
	v_cvt_f32_i32_e32 v21, v21
	v_cvt_f32_i32_e32 v20, v20
	v_rcp_f32_e32 v30, v30
	v_rcp_f32_e32 v31, v31
	v_pk_mul_f32 v[22:23], v[22:23], v[34:35] op_sel_hi:[1,0]
	v_pk_mul_f32 v[18:19], v[18:19], v[26:27]
	v_pk_mul_f32 v[22:23], v[22:23], v[38:39]
	v_pk_add_f32 v[26:27], v[32:33], 1.0 op_sel_hi:[1,0]
	v_pk_mul_f32 v[18:19], v[18:19], v[34:35] op_sel_hi:[1,0]
	v_pk_mul_f32 v[20:21], v[20:21], v[28:29]
	v_rcp_f32_e32 v26, v26
	v_rcp_f32_e32 v27, v27
	v_pk_mul_f32 v[18:19], v[18:19], v[30:31]
	v_med3_f32 v28, v22, s54, v221
	v_med3_f32 v23, v23, s54, v221
	v_cvt_pk_fp8_f32 v22, v28, v23
	v_med3_f32 v18, v18, s54, v221
	v_med3_f32 v19, v19, s54, v221
	v_cvt_pk_fp8_f32 v23, v18, v19
	v_pk_mul_f32 v[20:21], v[20:21], v[34:35] op_sel_hi:[1,0]
	v_cvt_f32_i32_e32 v17, v17
	v_pk_mul_f32 v[20:21], v[20:21], v[26:27]
	v_cvt_f32_i32_e32 v16, v16
	v_med3_f32 v18, v20, s54, v221
	v_med3_f32 v19, v21, s54, v221
	v_cvt_pk_fp8_f32 v23, v18, v19 op_sel:[0,0,1]
	v_pk_mul_f32 v[18:19], v[204:205], v[206:207] op_sel_hi:[1,0]
	v_cvt_f32_i32_e32 v15, v15
	v_mul_f32_e32 v20, 0xbfb8aa3b, v18
	v_pk_mul_f32 v[28:29], v[16:17], v[20:21] op_sel_hi:[1,0]
	v_cvt_f32_i32_e32 v14, v14
	v_cvt_f32_i32_e32 v11, v11
	v_cvt_f32_i32_e32 v10, v10
	v_cvt_f32_i32_e32 v7, v7
	v_cvt_f32_i32_e32 v6, v6
	v_cvt_f32_i32_e32 v9, v9
	v_cvt_f32_i32_e32 v8, v8
	v_exp_f32_e32 v28, v28
	v_exp_f32_e32 v29, v29
	v_med3_f32 v24, v24, s54, v221
	v_med3_f32 v25, v25, s54, v221
	v_cvt_pk_fp8_f32 v22, v24, v25 op_sel:[0,0,1]
	v_pk_mul_f32 v[24:25], v[14:15], v[20:21] op_sel_hi:[1,0]
	v_pk_mul_f32 v[8:9], v[8:9], v[16:17]
	v_pk_mul_f32 v[6:7], v[6:7], v[14:15]
	v_pk_add_f32 v[14:15], v[28:29], 1.0 op_sel_hi:[1,0]
	v_pk_mul_f32 v[16:17], v[10:11], v[20:21] op_sel_hi:[1,0]
	v_cvt_f32_i32_e32 v13, v13
	v_cvt_f32_i32_e32 v12, v12
	v_rcp_f32_e32 v14, v14
	v_rcp_f32_e32 v15, v15
	v_exp_f32_e32 v16, v16
	v_exp_f32_e32 v17, v17
	v_mul_f32_e32 v18, v18, v19
	v_mul_f32_e32 v18, 0x41000000, v18
	v_pk_mul_f32 v[8:9], v[8:9], v[18:19] op_sel_hi:[1,0]
	v_exp_f32_e32 v24, v24
	v_exp_f32_e32 v25, v25
	v_pk_mul_f32 v[8:9], v[8:9], v[14:15]
	v_pk_add_f32 v[14:15], v[16:17], 1.0 op_sel_hi:[1,0]
	v_pk_mul_f32 v[16:17], v[12:13], v[20:21] op_sel_hi:[1,0]
	v_cvt_f32_i32_e32 v3, v3
	v_cvt_f32_i32_e32 v2, v2
	v_exp_f32_e32 v16, v16
	v_exp_f32_e32 v17, v17
	v_cvt_f32_i32_e32 v5, v5
	v_cvt_f32_i32_e32 v4, v4
	v_pk_add_f32 v[24:25], v[24:25], 1.0 op_sel_hi:[1,0]
	v_pk_mul_f32 v[2:3], v[2:3], v[10:11]
	v_rcp_f32_e32 v24, v24
	v_rcp_f32_e32 v25, v25
	v_pk_add_f32 v[10:11], v[16:17], 1.0 op_sel_hi:[1,0]
	v_rcp_f32_e32 v14, v14
	v_rcp_f32_e32 v15, v15
	v_rcp_f32_e32 v10, v10
	v_rcp_f32_e32 v11, v11
	v_pk_mul_f32 v[6:7], v[6:7], v[18:19] op_sel_hi:[1,0]
	v_pk_mul_f32 v[4:5], v[4:5], v[12:13]
	v_pk_mul_f32 v[6:7], v[6:7], v[24:25]
	v_pk_mul_f32 v[2:3], v[2:3], v[18:19] op_sel_hi:[1,0]
	v_pk_mul_f32 v[4:5], v[4:5], v[18:19] op_sel_hi:[1,0]
	v_pk_mul_f32 v[2:3], v[2:3], v[14:15]
	v_pk_mul_f32 v[4:5], v[4:5], v[10:11]
	v_med3_f32 v10, v6, s54, v221
	v_med3_f32 v7, v7, s54, v221
	v_cvt_pk_fp8_f32 v6, v10, v7
	v_med3_f32 v2, v2, s54, v221
	v_med3_f32 v3, v3, s54, v221
	v_cvt_pk_fp8_f32 v7, v2, v3
	v_med3_f32 v8, v8, s54, v221
	v_med3_f32 v9, v9, s54, v221
	v_med3_f32 v2, v4, s54, v221
	v_med3_f32 v3, v5, s54, v221
	v_cvt_pk_fp8_f32 v6, v8, v9 op_sel:[0,0,1]
	v_cvt_pk_fp8_f32 v7, v2, v3 op_sel:[0,0,1]
	v_lshl_add_u64 v[58:59], s[18:19], 0, v[224:225]
	v_lshl_add_u64 v[26:27], s[18:19], 0, v[228:229]
	v_lshl_add_u64 v[2:3], s[18:19], 0, v[230:231]
	v_lshl_add_u64 v[58:59], v[58:59], 0, v[194:195]
	v_lshl_add_u64 v[26:27], v[26:27], 0, v[194:195]
	v_lshl_add_u64 v[2:3], v[2:3], 0, v[194:195]
	s_andn2_b64 vcc, exec, s[14:15]
	s_mov_b64 s[14:15], -1
	global_store_dwordx2 v[58:59], v[54:55], off
	global_store_dwordx2 v[26:27], v[22:23], off
	global_store_dwordx2 v[2:3], v[6:7], off
	s_cbranch_vccnz .LBB0_1201
	s_andn2_b64 vcc, exec, s[0:1]
	s_cbranch_vccnz .LBB0_1200
	s_barrier

.LBB0_1517:
	v_cvt_f32_i32_e32 v129, v129
	v_cvt_f32_i32_e32 v128, v128
	v_pk_mul_f32 v[130:131], v[204:205], v[220:221] op_sel_hi:[1,0]
	v_cvt_f32_i32_e32 v127, v127
	v_mul_f32_e32 v132, 0xbfb8aa3b, v130
	v_pk_mul_f32 v[136:137], v[128:129], v[132:133] op_sel_hi:[1,0]
	v_cvt_f32_i32_e32 v126, v126
	v_cvt_f32_i32_e32 v123, v123
	v_cvt_f32_i32_e32 v122, v122
	v_cvt_f32_i32_e32 v119, v119
	v_cvt_f32_i32_e32 v118, v118
	v_cvt_f32_i32_e32 v121, v121
	v_cvt_f32_i32_e32 v120, v120
	v_exp_f32_e32 v136, v136
	v_exp_f32_e32 v137, v137
	v_pk_mul_f32 v[134:135], v[126:127], v[132:133] op_sel_hi:[1,0]
	v_pk_mul_f32 v[120:121], v[120:121], v[128:129]
	v_pk_mul_f32 v[118:119], v[118:119], v[126:127]
	v_pk_add_f32 v[126:127], v[136:137], 1.0 op_sel_hi:[1,0]
	v_pk_mul_f32 v[128:129], v[122:123], v[132:133] op_sel_hi:[1,0]
	v_cvt_f32_i32_e32 v125, v125
	v_cvt_f32_i32_e32 v124, v124
	v_exp_f32_e32 v134, v134
	v_exp_f32_e32 v135, v135
	v_rcp_f32_e32 v126, v126
	v_rcp_f32_e32 v127, v127
	v_exp_f32_e32 v128, v128
	v_exp_f32_e32 v129, v129
	v_mul_f32_e32 v130, v130, v131
	v_mul_f32_e32 v130, 0x41000000, v130
	v_pk_mul_f32 v[120:121], v[120:121], v[130:131] op_sel_hi:[1,0]
	v_cvt_f32_i32_e32 v115, v115
	v_cvt_f32_i32_e32 v114, v114
	v_pk_add_f32 v[134:135], v[134:135], 1.0 op_sel_hi:[1,0]
	v_pk_mul_f32 v[120:121], v[120:121], v[126:127]
	v_pk_add_f32 v[126:127], v[128:129], 1.0 op_sel_hi:[1,0]
	v_pk_mul_f32 v[128:129], v[124:125], v[132:133] op_sel_hi:[1,0]
	v_cvt_f32_i32_e32 v117, v117
	v_cvt_f32_i32_e32 v116, v116
	v_rcp_f32_e32 v134, v134
	v_rcp_f32_e32 v135, v135
	v_exp_f32_e32 v128, v128
	v_exp_f32_e32 v129, v129
	v_rcp_f32_e32 v126, v126
	v_rcp_f32_e32 v127, v127
	v_pk_mul_f32 v[118:119], v[118:119], v[130:131] op_sel_hi:[1,0]
	v_pk_mul_f32 v[114:115], v[114:115], v[122:123]
	v_pk_mul_f32 v[118:119], v[118:119], v[134:135]
	v_pk_mul_f32 v[116:117], v[116:117], v[124:125]
	v_pk_add_f32 v[122:123], v[128:129], 1.0 op_sel_hi:[1,0]
	v_pk_mul_f32 v[114:115], v[114:115], v[130:131] op_sel_hi:[1,0]
	v_rcp_f32_e32 v122, v122
	v_rcp_f32_e32 v123, v123
	v_pk_mul_f32 v[124:125], v[114:115], v[126:127]
	v_pk_mul_f32 v[114:115], v[116:117], v[130:131] op_sel_hi:[1,0]
	v_med3_f32 v117, v118, s56, v209
	v_med3_f32 v118, v119, s56, v209
	v_cvt_pk_fp8_f32 v116, v117, v118
	v_med3_f32 v118, v120, s56, v209
	v_med3_f32 v119, v121, s56, v209
	v_med3_f32 v120, v124, s56, v209
	v_med3_f32 v121, v125, s56, v209
	v_cvt_pk_fp8_f32 v117, v120, v121
	v_pk_mul_f32 v[122:123], v[114:115], v[122:123]
	v_cvt_f32_i32_e32 v113, v113
	v_cvt_f32_i32_e32 v112, v112
	v_cvt_pk_fp8_f32 v116, v118, v119 op_sel:[0,0,1]
	v_med3_f32 v118, v122, s56, v209
	v_med3_f32 v119, v123, s56, v209
	v_cvt_pk_fp8_f32 v117, v118, v119 op_sel:[0,0,1]
	v_pk_mul_f32 v[118:119], v[204:205], v[218:219] op_sel_hi:[1,0]
	v_cvt_f32_i32_e32 v111, v111
	v_mul_f32_e32 v120, 0xbfb8aa3b, v118
	v_pk_mul_f32 v[124:125], v[112:113], v[120:121] op_sel_hi:[1,0]
	v_cvt_f32_i32_e32 v110, v110
	v_cvt_f32_i32_e32 v107, v107
	v_cvt_f32_i32_e32 v106, v106
	v_cvt_f32_i32_e32 v103, v103
	v_cvt_f32_i32_e32 v102, v102
	v_cvt_f32_i32_e32 v105, v105
	v_cvt_f32_i32_e32 v104, v104
	v_exp_f32_e32 v124, v124
	v_exp_f32_e32 v125, v125
	v_pk_mul_f32 v[122:123], v[110:111], v[120:121] op_sel_hi:[1,0]
	v_pk_mul_f32 v[104:105], v[104:105], v[112:113]
	v_pk_mul_f32 v[102:103], v[102:103], v[110:111]
	v_pk_add_f32 v[110:111], v[124:125], 1.0 op_sel_hi:[1,0]
	v_pk_mul_f32 v[112:113], v[106:107], v[120:121] op_sel_hi:[1,0]
	v_cvt_f32_i32_e32 v109, v109
	v_cvt_f32_i32_e32 v108, v108
	v_rcp_f32_e32 v110, v110
	v_rcp_f32_e32 v111, v111
	v_exp_f32_e32 v112, v112
	v_exp_f32_e32 v113, v113
	v_mul_f32_e32 v118, v118, v119
	v_mul_f32_e32 v118, 0x41000000, v118
	v_pk_mul_f32 v[104:105], v[104:105], v[118:119] op_sel_hi:[1,0]
	v_exp_f32_e32 v122, v122
	v_exp_f32_e32 v123, v123
	v_pk_mul_f32 v[104:105], v[104:105], v[110:111]
	v_pk_add_f32 v[110:111], v[112:113], 1.0 op_sel_hi:[1,0]
	v_pk_mul_f32 v[112:113], v[108:109], v[120:121] op_sel_hi:[1,0]
	v_cvt_f32_i32_e32 v99, v99
	v_cvt_f32_i32_e32 v98, v98
	v_exp_f32_e32 v112, v112
	v_exp_f32_e32 v113, v113
	v_cvt_f32_i32_e32 v101, v101
	v_cvt_f32_i32_e32 v100, v100
	v_pk_add_f32 v[122:123], v[122:123], 1.0 op_sel_hi:[1,0]
	v_rcp_f32_e32 v110, v110
	v_rcp_f32_e32 v122, v122
	v_rcp_f32_e32 v123, v123
	v_rcp_f32_e32 v111, v111
	v_pk_mul_f32 v[98:99], v[98:99], v[106:107]
	v_pk_add_f32 v[106:107], v[112:113], 1.0 op_sel_hi:[1,0]
	v_pk_mul_f32 v[102:103], v[102:103], v[118:119] op_sel_hi:[1,0]
	v_rcp_f32_e32 v106, v106
	v_rcp_f32_e32 v107, v107
	v_pk_mul_f32 v[100:101], v[100:101], v[108:109]
	v_pk_mul_f32 v[98:99], v[98:99], v[118:119] op_sel_hi:[1,0]
	v_pk_mul_f32 v[102:103], v[102:103], v[122:123]
	v_pk_mul_f32 v[108:109], v[98:99], v[110:111]
	v_pk_mul_f32 v[98:99], v[100:101], v[118:119] op_sel_hi:[1,0]
	v_cvt_f32_i32_e32 v97, v97
	v_pk_mul_f32 v[100:101], v[98:99], v[106:107]
	v_med3_f32 v99, v102, s56, v209
	v_med3_f32 v102, v103, s56, v209
	v_cvt_pk_fp8_f32 v98, v99, v102
	v_med3_f32 v102, v104, s56, v209
	v_med3_f32 v103, v105, s56, v209
	v_med3_f32 v104, v108, s56, v209
	v_med3_f32 v105, v109, s56, v209
	v_cvt_pk_fp8_f32 v99, v104, v105
	v_cvt_f32_i32_e32 v96, v96
	v_med3_f32 v100, v100, s56, v209
	v_med3_f32 v101, v101, s56, v209
	v_cvt_pk_fp8_f32 v99, v100, v101 op_sel:[0,0,1]
	v_pk_mul_f32 v[100:101], v[204:205], v[216:217] op_sel_hi:[1,0]
	v_cvt_pk_fp8_f32 v98, v102, v103 op_sel:[0,0,1]
	v_mul_f32_e32 v102, 0xbfb8aa3b, v100
	v_pk_mul_f32 v[106:107], v[96:97], v[102:103] op_sel_hi:[1,0]
	v_cvt_f32_i32_e32 v95, v95
	v_cvt_f32_i32_e32 v94, v94
	v_cvt_f32_i32_e32 v91, v91
	v_cvt_f32_i32_e32 v90, v90
	v_cvt_f32_i32_e32 v87, v87
	v_cvt_f32_i32_e32 v86, v86
	v_cvt_f32_i32_e32 v89, v89
	v_cvt_f32_i32_e32 v88, v88
	v_exp_f32_e32 v106, v106
	v_exp_f32_e32 v107, v107
	v_pk_mul_f32 v[104:105], v[94:95], v[102:103] op_sel_hi:[1,0]
	v_pk_mul_f32 v[88:89], v[88:89], v[96:97]
	v_pk_mul_f32 v[86:87], v[86:87], v[94:95]
	v_pk_add_f32 v[94:95], v[106:107], 1.0 op_sel_hi:[1,0]
	v_pk_mul_f32 v[96:97], v[90:91], v[102:103] op_sel_hi:[1,0]
	v_cvt_f32_i32_e32 v93, v93
	v_cvt_f32_i32_e32 v92, v92
	v_rcp_f32_e32 v94, v94
	v_rcp_f32_e32 v95, v95
	v_exp_f32_e32 v96, v96
	v_exp_f32_e32 v97, v97
	v_mul_f32_e32 v100, v100, v101
	v_mul_f32_e32 v100, 0x41000000, v100
	v_pk_mul_f32 v[88:89], v[88:89], v[100:101] op_sel_hi:[1,0]
	v_exp_f32_e32 v104, v104
	v_exp_f32_e32 v105, v105
	v_pk_mul_f32 v[88:89], v[88:89], v[94:95]
	v_pk_add_f32 v[94:95], v[96:97], 1.0 op_sel_hi:[1,0]
	v_pk_mul_f32 v[96:97], v[92:93], v[102:103] op_sel_hi:[1,0]
	v_cvt_f32_i32_e32 v83, v83
	v_cvt_f32_i32_e32 v82, v82
	v_exp_f32_e32 v96, v96
	v_exp_f32_e32 v97, v97
	v_cvt_f32_i32_e32 v85, v85
	v_cvt_f32_i32_e32 v84, v84
	v_pk_add_f32 v[104:105], v[104:105], 1.0 op_sel_hi:[1,0]
	v_pk_mul_f32 v[82:83], v[82:83], v[90:91]
	v_rcp_f32_e32 v104, v104
	v_rcp_f32_e32 v105, v105
	v_pk_add_f32 v[90:91], v[96:97], 1.0 op_sel_hi:[1,0]
	v_rcp_f32_e32 v94, v94
	v_rcp_f32_e32 v95, v95
	v_rcp_f32_e32 v90, v90
	v_rcp_f32_e32 v91, v91
	v_pk_mul_f32 v[86:87], v[86:87], v[100:101] op_sel_hi:[1,0]
	v_pk_mul_f32 v[84:85], v[84:85], v[92:93]
	v_pk_mul_f32 v[86:87], v[86:87], v[104:105]
	v_pk_mul_f32 v[82:83], v[82:83], v[100:101] op_sel_hi:[1,0]
	v_pk_mul_f32 v[84:85], v[84:85], v[100:101] op_sel_hi:[1,0]
	v_pk_mul_f32 v[82:83], v[82:83], v[94:95]
	v_pk_mul_f32 v[84:85], v[84:85], v[90:91]
	v_med3_f32 v90, v86, s56, v209
	v_med3_f32 v87, v87, s56, v209
	v_cvt_pk_fp8_f32 v86, v90, v87
	v_med3_f32 v82, v82, s56, v209
	v_med3_f32 v83, v83, s56, v209
	v_cvt_pk_fp8_f32 v87, v82, v83
	v_cvt_f32_i32_e32 v81, v81
	v_cvt_f32_i32_e32 v80, v80
	v_med3_f32 v82, v84, s56, v209
	v_med3_f32 v83, v85, s56, v209
	v_cvt_pk_fp8_f32 v87, v82, v83 op_sel:[0,0,1]
	v_pk_mul_f32 v[82:83], v[204:205], v[214:215] op_sel_hi:[1,0]
	v_cvt_f32_i32_e32 v79, v79
	v_mul_f32_e32 v84, 0xbfb8aa3b, v82
	v_pk_mul_f32 v[90:91], v[80:81], v[84:85] op_sel_hi:[1,0]
	v_cvt_f32_i32_e32 v78, v78
	v_cvt_f32_i32_e32 v75, v75
	v_cvt_f32_i32_e32 v74, v74
	v_cvt_f32_i32_e32 v71, v71
	v_cvt_f32_i32_e32 v70, v70
	v_cvt_f32_i32_e32 v73, v73
	v_cvt_f32_i32_e32 v72, v72
	v_exp_f32_e32 v90, v90
	v_exp_f32_e32 v91, v91
	v_med3_f32 v88, v88, s56, v209
	v_med3_f32 v89, v89, s56, v209
	v_cvt_pk_fp8_f32 v86, v88, v89 op_sel:[0,0,1]
	v_pk_mul_f32 v[88:89], v[78:79], v[84:85] op_sel_hi:[1,0]
	v_pk_mul_f32 v[72:73], v[72:73], v[80:81]
	v_pk_mul_f32 v[70:71], v[70:71], v[78:79]
	v_pk_add_f32 v[78:79], v[90:91], 1.0 op_sel_hi:[1,0]
	v_pk_mul_f32 v[80:81], v[74:75], v[84:85] op_sel_hi:[1,0]
	v_cvt_f32_i32_e32 v77, v77
	v_cvt_f32_i32_e32 v76, v76
	v_rcp_f32_e32 v78, v78
	v_rcp_f32_e32 v79, v79
	v_exp_f32_e32 v80, v80
	v_exp_f32_e32 v81, v81
	v_mul_f32_e32 v82, v82, v83
	v_mul_f32_e32 v82, 0x41000000, v82
	v_pk_mul_f32 v[72:73], v[72:73], v[82:83] op_sel_hi:[1,0]
	v_exp_f32_e32 v88, v88
	v_exp_f32_e32 v89, v89
	v_pk_mul_f32 v[72:73], v[72:73], v[78:79]
	v_pk_add_f32 v[78:79], v[80:81], 1.0 op_sel_hi:[1,0]
	v_pk_mul_f32 v[80:81], v[76:77], v[84:85] op_sel_hi:[1,0]
	v_cvt_f32_i32_e32 v67, v67
	v_cvt_f32_i32_e32 v66, v66
	v_exp_f32_e32 v80, v80
	v_exp_f32_e32 v81, v81
	v_cvt_f32_i32_e32 v69, v69
	v_cvt_f32_i32_e32 v68, v68
	v_pk_add_f32 v[88:89], v[88:89], 1.0 op_sel_hi:[1,0]
	v_pk_mul_f32 v[66:67], v[66:67], v[74:75]
	v_rcp_f32_e32 v88, v88
	v_rcp_f32_e32 v89, v89
	v_pk_add_f32 v[74:75], v[80:81], 1.0 op_sel_hi:[1,0]
	v_rcp_f32_e32 v78, v78
	v_rcp_f32_e32 v79, v79
	v_rcp_f32_e32 v74, v74
	v_rcp_f32_e32 v75, v75
	v_pk_mul_f32 v[70:71], v[70:71], v[82:83] op_sel_hi:[1,0]
	v_pk_mul_f32 v[68:69], v[68:69], v[76:77]
	v_pk_mul_f32 v[70:71], v[70:71], v[88:89]
	v_pk_mul_f32 v[66:67], v[66:67], v[82:83] op_sel_hi:[1,0]
	v_pk_mul_f32 v[68:69], v[68:69], v[82:83] op_sel_hi:[1,0]
	v_pk_mul_f32 v[66:67], v[66:67], v[78:79]
	v_pk_mul_f32 v[68:69], v[68:69], v[74:75]
	v_med3_f32 v74, v70, s56, v209
	v_med3_f32 v71, v71, s56, v209
	v_cvt_pk_fp8_f32 v70, v74, v71
	v_med3_f32 v66, v66, s56, v209
	v_med3_f32 v67, v67, s56, v209
	v_cvt_pk_fp8_f32 v71, v66, v67
	s_lshl_b32 s9, s20, 2
	s_or_b32 s20, s9, s51
	v_cvt_f32_i32_e32 v65, v65
	v_cvt_f32_i32_e32 v64, v64
	s_ashr_i32 s21, s20, 31
	v_med3_f32 v66, v68, s56, v209
	v_med3_f32 v67, v69, s56, v209
	s_lshl_b64 s[20:21], s[20:21], 13
	s_mul_i32 s11, s18, 0x160000
	v_cvt_pk_fp8_f32 v71, v66, v67 op_sel:[0,0,1]
	v_pk_mul_f32 v[66:67], v[204:205], v[212:213] op_sel_hi:[1,0]
	s_mul_hi_i32 s9, s18, 0x160000
	s_add_u32 s11, s33, s11
	v_med3_f32 v72, v72, s56, v209
	v_med3_f32 v73, v73, s56, v209
	v_mul_f32_e32 v68, 0xbfb8aa3b, v66
	s_addc_u32 s9, s42, s9
	v_cvt_pk_fp8_f32 v70, v72, v73 op_sel:[0,0,1]
	v_pk_mul_f32 v[72:73], v[64:65], v[68:69] op_sel_hi:[1,0]
	s_add_u32 s18, s11, s20
	v_cvt_f32_i32_e32 v63, v63
	v_cvt_f32_i32_e32 v62, v62
	v_cvt_f32_i32_e32 v59, v59
	v_cvt_f32_i32_e32 v58, v58
	v_cvt_f32_i32_e32 v55, v55
	v_cvt_f32_i32_e32 v54, v54
	v_cvt_f32_i32_e32 v57, v57
	v_cvt_f32_i32_e32 v56, v56
	v_exp_f32_e32 v72, v72
	v_exp_f32_e32 v73, v73
	s_addc_u32 s19, s9, s21
	v_lshl_add_u64 v[114:115], s[18:19], 0, v[222:223]
	v_lshl_add_u64 v[114:115], v[114:115], 0, v[194:195]
	global_store_dwordx2 v[114:115], v[116:117], off
	global_store_dwordx2 v[114:115], v[98:99], off offset:512
	global_store_dwordx2 v[114:115], v[86:87], off offset:1024
	global_store_dwordx2 v[114:115], v[70:71], off offset:1536
	v_pk_mul_f32 v[70:71], v[62:63], v[68:69] op_sel_hi:[1,0]
	v_pk_mul_f32 v[56:57], v[56:57], v[64:65]
	v_pk_mul_f32 v[54:55], v[54:55], v[62:63]
	v_pk_add_f32 v[62:63], v[72:73], 1.0 op_sel_hi:[1,0]
	v_pk_mul_f32 v[64:65], v[58:59], v[68:69] op_sel_hi:[1,0]
	v_cvt_f32_i32_e32 v61, v61
	v_cvt_f32_i32_e32 v60, v60
	v_exp_f32_e32 v70, v70
	v_exp_f32_e32 v71, v71
	v_rcp_f32_e32 v62, v62
	v_rcp_f32_e32 v63, v63
	v_exp_f32_e32 v64, v64
	v_exp_f32_e32 v65, v65
	v_mul_f32_e32 v66, v66, v67
	v_mul_f32_e32 v66, 0x41000000, v66
	v_pk_mul_f32 v[56:57], v[56:57], v[66:67] op_sel_hi:[1,0]
	v_cvt_f32_i32_e32 v51, v51
	v_cvt_f32_i32_e32 v50, v50
	v_pk_add_f32 v[70:71], v[70:71], 1.0 op_sel_hi:[1,0]
	v_pk_mul_f32 v[56:57], v[56:57], v[62:63]
	v_pk_add_f32 v[62:63], v[64:65], 1.0 op_sel_hi:[1,0]
	v_pk_mul_f32 v[64:65], v[60:61], v[68:69] op_sel_hi:[1,0]
	v_rcp_f32_e32 v70, v70
	v_rcp_f32_e32 v71, v71
	v_exp_f32_e32 v64, v64
	v_exp_f32_e32 v65, v65
	v_cvt_f32_i32_e32 v53, v53
	v_cvt_f32_i32_e32 v52, v52
	v_rcp_f32_e32 v62, v62
	v_rcp_f32_e32 v63, v63
	v_pk_mul_f32 v[54:55], v[54:55], v[66:67] op_sel_hi:[1,0]
	v_pk_mul_f32 v[50:51], v[50:51], v[58:59]
	v_pk_mul_f32 v[54:55], v[54:55], v[70:71]
	v_pk_add_f32 v[58:59], v[64:65], 1.0 op_sel_hi:[1,0]
	v_pk_mul_f32 v[50:51], v[50:51], v[66:67] op_sel_hi:[1,0]
	v_pk_mul_f32 v[52:53], v[52:53], v[60:61]
	v_rcp_f32_e32 v58, v58
	v_rcp_f32_e32 v59, v59
	v_pk_mul_f32 v[50:51], v[50:51], v[62:63]
	v_med3_f32 v60, v54, s56, v209
	v_med3_f32 v55, v55, s56, v209
	v_cvt_pk_fp8_f32 v54, v60, v55
	v_med3_f32 v50, v50, s56, v209
	v_med3_f32 v51, v51, s56, v209
	v_cvt_pk_fp8_f32 v55, v50, v51
	v_pk_mul_f32 v[52:53], v[52:53], v[66:67] op_sel_hi:[1,0]
	v_cvt_f32_i32_e32 v49, v49
	v_pk_mul_f32 v[52:53], v[52:53], v[58:59]
	v_cvt_f32_i32_e32 v48, v48
	v_med3_f32 v50, v52, s56, v209
	v_med3_f32 v51, v53, s56, v209
	v_cvt_pk_fp8_f32 v55, v50, v51 op_sel:[0,0,1]
	v_pk_mul_f32 v[50:51], v[204:205], v[210:211] op_sel_hi:[1,0]
	v_cvt_f32_i32_e32 v47, v47
	v_mul_f32_e32 v52, 0xbfb8aa3b, v50
	v_pk_mul_f32 v[60:61], v[48:49], v[52:53] op_sel_hi:[1,0]
	v_cvt_f32_i32_e32 v46, v46
	v_cvt_f32_i32_e32 v43, v43
	v_cvt_f32_i32_e32 v42, v42
	v_cvt_f32_i32_e32 v39, v39
	v_cvt_f32_i32_e32 v38, v38
	v_cvt_f32_i32_e32 v41, v41
	v_cvt_f32_i32_e32 v40, v40
	v_exp_f32_e32 v60, v60
	v_exp_f32_e32 v61, v61
	v_med3_f32 v56, v56, s56, v209
	v_med3_f32 v57, v57, s56, v209
	v_cvt_pk_fp8_f32 v54, v56, v57 op_sel:[0,0,1]
	v_pk_mul_f32 v[56:57], v[46:47], v[52:53] op_sel_hi:[1,0]
	v_pk_mul_f32 v[40:41], v[40:41], v[48:49]
	v_pk_mul_f32 v[38:39], v[38:39], v[46:47]
	v_pk_add_f32 v[46:47], v[60:61], 1.0 op_sel_hi:[1,0]
	v_pk_mul_f32 v[48:49], v[42:43], v[52:53] op_sel_hi:[1,0]
	v_cvt_f32_i32_e32 v45, v45
	v_cvt_f32_i32_e32 v44, v44
	v_rcp_f32_e32 v46, v46
	v_rcp_f32_e32 v47, v47
	v_exp_f32_e32 v48, v48
	v_exp_f32_e32 v49, v49
	v_mul_f32_e32 v50, v50, v51
	v_mul_f32_e32 v50, 0x41000000, v50
	v_pk_mul_f32 v[40:41], v[40:41], v[50:51] op_sel_hi:[1,0]
	v_exp_f32_e32 v56, v56
	v_exp_f32_e32 v57, v57
	v_pk_mul_f32 v[40:41], v[40:41], v[46:47]
	v_pk_add_f32 v[46:47], v[48:49], 1.0 op_sel_hi:[1,0]
	v_pk_mul_f32 v[48:49], v[44:45], v[52:53] op_sel_hi:[1,0]
	v_cvt_f32_i32_e32 v35, v35
	v_cvt_f32_i32_e32 v34, v34
	v_exp_f32_e32 v48, v48
	v_exp_f32_e32 v49, v49
	v_cvt_f32_i32_e32 v37, v37
	v_cvt_f32_i32_e32 v36, v36
	v_pk_add_f32 v[56:57], v[56:57], 1.0 op_sel_hi:[1,0]
	v_pk_mul_f32 v[34:35], v[34:35], v[42:43]
	v_rcp_f32_e32 v56, v56
	v_rcp_f32_e32 v57, v57
	v_pk_add_f32 v[42:43], v[48:49], 1.0 op_sel_hi:[1,0]
	v_rcp_f32_e32 v46, v46
	v_rcp_f32_e32 v47, v47
	v_rcp_f32_e32 v42, v42
	v_rcp_f32_e32 v43, v43
	v_pk_mul_f32 v[38:39], v[38:39], v[50:51] op_sel_hi:[1,0]
	v_pk_mul_f32 v[36:37], v[36:37], v[44:45]
	v_pk_mul_f32 v[38:39], v[38:39], v[56:57]
	v_pk_mul_f32 v[34:35], v[34:35], v[50:51] op_sel_hi:[1,0]
	v_pk_mul_f32 v[36:37], v[36:37], v[50:51] op_sel_hi:[1,0]
	v_pk_mul_f32 v[34:35], v[34:35], v[46:47]
	v_pk_mul_f32 v[36:37], v[36:37], v[42:43]
	v_med3_f32 v42, v38, s56, v209
	v_med3_f32 v39, v39, s56, v209
	v_cvt_pk_fp8_f32 v38, v42, v39
	v_med3_f32 v34, v34, s56, v209
	v_med3_f32 v35, v35, s56, v209
	v_cvt_pk_fp8_f32 v39, v34, v35
	v_med3_f32 v40, v40, s56, v209
	v_med3_f32 v41, v41, s56, v209
	v_med3_f32 v34, v36, s56, v209
	v_med3_f32 v35, v37, s56, v209
	v_cvt_pk_fp8_f32 v38, v40, v41 op_sel:[0,0,1]
	v_cvt_pk_fp8_f32 v39, v34, v35 op_sel:[0,0,1]
	v_lshl_add_u64 v[34:35], s[18:19], 0, v[226:227]
	v_cvt_f32_i32_e32 v33, v33
	v_cvt_f32_i32_e32 v32, v32
	v_lshl_add_u64 v[34:35], v[34:35], 0, v[194:195]
	global_store_dwordx2 v[34:35], v[38:39], off
	v_pk_mul_f32 v[34:35], v[204:205], v[208:209] op_sel_hi:[1,0]
	v_cvt_f32_i32_e32 v31, v31
	v_mul_f32_e32 v36, 0xbfb8aa3b, v34
	v_pk_mul_f32 v[40:41], v[32:33], v[36:37] op_sel_hi:[1,0]
	v_cvt_f32_i32_e32 v30, v30
	v_cvt_f32_i32_e32 v27, v27
	v_cvt_f32_i32_e32 v26, v26
	v_cvt_f32_i32_e32 v23, v23
	v_cvt_f32_i32_e32 v22, v22
	v_cvt_f32_i32_e32 v25, v25
	v_cvt_f32_i32_e32 v24, v24
	v_exp_f32_e32 v40, v40
	v_exp_f32_e32 v41, v41
	v_pk_mul_f32 v[38:39], v[30:31], v[36:37] op_sel_hi:[1,0]
	v_pk_mul_f32 v[24:25], v[24:25], v[32:33]
	v_pk_mul_f32 v[22:23], v[22:23], v[30:31]
	v_pk_add_f32 v[30:31], v[40:41], 1.0 op_sel_hi:[1,0]
	v_pk_mul_f32 v[32:33], v[26:27], v[36:37] op_sel_hi:[1,0]
	v_cvt_f32_i32_e32 v29, v29
	v_cvt_f32_i32_e32 v28, v28
	v_exp_f32_e32 v38, v38
	v_exp_f32_e32 v39, v39
	v_rcp_f32_e32 v30, v30
	v_rcp_f32_e32 v31, v31
	v_exp_f32_e32 v32, v32
	v_exp_f32_e32 v33, v33
	v_mul_f32_e32 v34, v34, v35
	v_mul_f32_e32 v34, 0x41000000, v34
	v_pk_mul_f32 v[24:25], v[24:25], v[34:35] op_sel_hi:[1,0]
	v_cvt_f32_i32_e32 v19, v19
	v_cvt_f32_i32_e32 v18, v18
	v_pk_add_f32 v[38:39], v[38:39], 1.0 op_sel_hi:[1,0]
	v_pk_mul_f32 v[24:25], v[24:25], v[30:31]
	v_pk_add_f32 v[30:31], v[32:33], 1.0 op_sel_hi:[1,0]
	v_pk_mul_f32 v[32:33], v[28:29], v[36:37] op_sel_hi:[1,0]
	v_rcp_f32_e32 v38, v38
	v_rcp_f32_e32 v39, v39
	v_exp_f32_e32 v32, v32
	v_exp_f32_e32 v33, v33
	v_cvt_f32_i32_e32 v21, v21
	v_cvt_f32_i32_e32 v20, v20
	v_rcp_f32_e32 v30, v30
	v_rcp_f32_e32 v31, v31
	v_pk_mul_f32 v[22:23], v[22:23], v[34:35] op_sel_hi:[1,0]
	v_pk_mul_f32 v[18:19], v[18:19], v[26:27]
	v_pk_mul_f32 v[22:23], v[22:23], v[38:39]
	v_pk_add_f32 v[26:27], v[32:33], 1.0 op_sel_hi:[1,0]
	v_pk_mul_f32 v[18:19], v[18:19], v[34:35] op_sel_hi:[1,0]
	v_pk_mul_f32 v[20:21], v[20:21], v[28:29]
	v_rcp_f32_e32 v26, v26
	v_rcp_f32_e32 v27, v27
	v_pk_mul_f32 v[18:19], v[18:19], v[30:31]
	v_med3_f32 v28, v22, s56, v209
	v_med3_f32 v23, v23, s56, v209
	v_cvt_pk_fp8_f32 v22, v28, v23
	v_med3_f32 v18, v18, s56, v209
	v_med3_f32 v19, v19, s56, v209
	v_cvt_pk_fp8_f32 v23, v18, v19
	v_pk_mul_f32 v[20:21], v[20:21], v[34:35] op_sel_hi:[1,0]
	v_cvt_f32_i32_e32 v17, v17
	v_pk_mul_f32 v[20:21], v[20:21], v[26:27]
	v_cvt_f32_i32_e32 v16, v16
	v_med3_f32 v18, v20, s56, v209
	v_med3_f32 v19, v21, s56, v209
	v_cvt_pk_fp8_f32 v23, v18, v19 op_sel:[0,0,1]
	v_pk_mul_f32 v[18:19], v[204:205], v[206:207] op_sel_hi:[1,0]
	v_cvt_f32_i32_e32 v15, v15
	v_mul_f32_e32 v20, 0xbfb8aa3b, v18
	v_pk_mul_f32 v[28:29], v[16:17], v[20:21] op_sel_hi:[1,0]
	v_cvt_f32_i32_e32 v14, v14
	v_cvt_f32_i32_e32 v11, v11
	v_cvt_f32_i32_e32 v10, v10
	v_cvt_f32_i32_e32 v7, v7
	v_cvt_f32_i32_e32 v6, v6
	v_cvt_f32_i32_e32 v9, v9
	v_cvt_f32_i32_e32 v8, v8
	v_exp_f32_e32 v28, v28
	v_exp_f32_e32 v29, v29
	v_med3_f32 v24, v24, s56, v209
	v_med3_f32 v25, v25, s56, v209
	v_cvt_pk_fp8_f32 v22, v24, v25 op_sel:[0,0,1]
	v_pk_mul_f32 v[24:25], v[14:15], v[20:21] op_sel_hi:[1,0]
	v_pk_mul_f32 v[8:9], v[8:9], v[16:17]
	v_pk_mul_f32 v[6:7], v[6:7], v[14:15]
	v_pk_add_f32 v[14:15], v[28:29], 1.0 op_sel_hi:[1,0]
	v_pk_mul_f32 v[16:17], v[10:11], v[20:21] op_sel_hi:[1,0]
	v_cvt_f32_i32_e32 v13, v13
	v_cvt_f32_i32_e32 v12, v12
	v_rcp_f32_e32 v14, v14
	v_rcp_f32_e32 v15, v15
	v_exp_f32_e32 v16, v16
	v_exp_f32_e32 v17, v17
	v_mul_f32_e32 v18, v18, v19
	v_mul_f32_e32 v18, 0x41000000, v18
	v_pk_mul_f32 v[8:9], v[8:9], v[18:19] op_sel_hi:[1,0]
	v_exp_f32_e32 v24, v24
	v_exp_f32_e32 v25, v25
	v_pk_mul_f32 v[8:9], v[8:9], v[14:15]
	v_pk_add_f32 v[14:15], v[16:17], 1.0 op_sel_hi:[1,0]
	v_pk_mul_f32 v[16:17], v[12:13], v[20:21] op_sel_hi:[1,0]
	v_cvt_f32_i32_e32 v3, v3
	v_cvt_f32_i32_e32 v2, v2
	v_exp_f32_e32 v16, v16
	v_exp_f32_e32 v17, v17
	v_cvt_f32_i32_e32 v5, v5
	v_cvt_f32_i32_e32 v4, v4
	v_pk_add_f32 v[24:25], v[24:25], 1.0 op_sel_hi:[1,0]
	v_pk_mul_f32 v[2:3], v[2:3], v[10:11]
	v_rcp_f32_e32 v24, v24
	v_rcp_f32_e32 v25, v25
	v_pk_add_f32 v[10:11], v[16:17], 1.0 op_sel_hi:[1,0]
	v_rcp_f32_e32 v14, v14
	v_rcp_f32_e32 v15, v15
	v_rcp_f32_e32 v10, v10
	v_rcp_f32_e32 v11, v11
	v_pk_mul_f32 v[6:7], v[6:7], v[18:19] op_sel_hi:[1,0]
	v_pk_mul_f32 v[4:5], v[4:5], v[12:13]
	v_pk_mul_f32 v[6:7], v[6:7], v[24:25]
	v_pk_mul_f32 v[2:3], v[2:3], v[18:19] op_sel_hi:[1,0]
	v_pk_mul_f32 v[4:5], v[4:5], v[18:19] op_sel_hi:[1,0]
	v_pk_mul_f32 v[2:3], v[2:3], v[14:15]
	v_pk_mul_f32 v[4:5], v[4:5], v[10:11]
	v_med3_f32 v10, v6, s56, v209
	v_med3_f32 v7, v7, s56, v209
	v_cvt_pk_fp8_f32 v6, v10, v7
	v_med3_f32 v2, v2, s56, v209
	v_med3_f32 v3, v3, s56, v209
	v_cvt_pk_fp8_f32 v7, v2, v3
	v_med3_f32 v8, v8, s56, v209
	v_med3_f32 v9, v9, s56, v209
	v_med3_f32 v2, v4, s56, v209
	v_med3_f32 v3, v5, s56, v209
	v_cvt_pk_fp8_f32 v6, v8, v9 op_sel:[0,0,1]
	v_cvt_pk_fp8_f32 v7, v2, v3 op_sel:[0,0,1]
	v_lshl_add_u64 v[58:59], s[18:19], 0, v[224:225]
	v_lshl_add_u64 v[26:27], s[18:19], 0, v[228:229]
	v_lshl_add_u64 v[2:3], s[18:19], 0, v[230:231]
	v_lshl_add_u64 v[58:59], v[58:59], 0, v[194:195]
	v_lshl_add_u64 v[26:27], v[26:27], 0, v[194:195]
	v_lshl_add_u64 v[2:3], v[2:3], 0, v[194:195]
	s_andn2_b64 vcc, exec, s[14:15]
	s_mov_b64 s[14:15], -1
	global_store_dwordx2 v[58:59], v[54:55], off
	global_store_dwordx2 v[26:27], v[22:23], off
	global_store_dwordx2 v[2:3], v[6:7], off
	s_cbranch_vccnz .LBB0_1498
	s_andn2_b64 vcc, exec, s[0:1]
	s_cbranch_vccnz .LBB0_1497
	s_barrier
	s_branch .LBB0_1497

.LBB0_3843:
	v_cvt_f32_i32_e32 v129, v129
	v_cvt_f32_i32_e32 v128, v128
	v_pk_mul_f32 v[130:131], v[204:205], v[222:223] op_sel_hi:[1,0]
	v_cvt_f32_i32_e32 v127, v127
	v_mul_f32_e32 v132, 0xbfb8aa3b, v130
	v_pk_mul_f32 v[136:137], v[128:129], v[132:133] op_sel_hi:[1,0]
	v_cvt_f32_i32_e32 v126, v126
	v_cvt_f32_i32_e32 v123, v123
	v_cvt_f32_i32_e32 v122, v122
	v_cvt_f32_i32_e32 v119, v119
	v_cvt_f32_i32_e32 v118, v118
	v_cvt_f32_i32_e32 v121, v121
	v_cvt_f32_i32_e32 v120, v120
	v_exp_f32_e32 v136, v136
	v_exp_f32_e32 v137, v137
	v_pk_mul_f32 v[134:135], v[126:127], v[132:133] op_sel_hi:[1,0]
	v_pk_mul_f32 v[120:121], v[120:121], v[128:129]
	v_pk_mul_f32 v[118:119], v[118:119], v[126:127]
	v_pk_add_f32 v[126:127], v[136:137], 1.0 op_sel_hi:[1,0]
	v_pk_mul_f32 v[128:129], v[122:123], v[132:133] op_sel_hi:[1,0]
	v_cvt_f32_i32_e32 v125, v125
	v_cvt_f32_i32_e32 v124, v124
	v_exp_f32_e32 v134, v134
	v_exp_f32_e32 v135, v135
	v_rcp_f32_e32 v126, v126
	v_rcp_f32_e32 v127, v127
	v_exp_f32_e32 v128, v128
	v_exp_f32_e32 v129, v129
	v_mul_f32_e32 v130, v130, v131
	v_mul_f32_e32 v130, 0x41000000, v130
	v_pk_mul_f32 v[120:121], v[120:121], v[130:131] op_sel_hi:[1,0]
	v_cvt_f32_i32_e32 v115, v115
	v_cvt_f32_i32_e32 v114, v114
	v_pk_add_f32 v[134:135], v[134:135], 1.0 op_sel_hi:[1,0]
	v_pk_mul_f32 v[120:121], v[120:121], v[126:127]
	v_pk_add_f32 v[126:127], v[128:129], 1.0 op_sel_hi:[1,0]
	v_pk_mul_f32 v[128:129], v[124:125], v[132:133] op_sel_hi:[1,0]
	v_cvt_f32_i32_e32 v117, v117
	v_cvt_f32_i32_e32 v116, v116
	v_rcp_f32_e32 v134, v134
	v_rcp_f32_e32 v135, v135
	v_exp_f32_e32 v128, v128
	v_exp_f32_e32 v129, v129
	v_rcp_f32_e32 v126, v126
	v_rcp_f32_e32 v127, v127
	v_pk_mul_f32 v[118:119], v[118:119], v[130:131] op_sel_hi:[1,0]
	v_pk_mul_f32 v[114:115], v[114:115], v[122:123]
	v_pk_mul_f32 v[118:119], v[118:119], v[134:135]
	v_pk_mul_f32 v[116:117], v[116:117], v[124:125]
	v_pk_add_f32 v[122:123], v[128:129], 1.0 op_sel_hi:[1,0]
	v_pk_mul_f32 v[114:115], v[114:115], v[130:131] op_sel_hi:[1,0]
	v_rcp_f32_e32 v122, v122
	v_rcp_f32_e32 v123, v123
	v_pk_mul_f32 v[124:125], v[114:115], v[126:127]
	v_pk_mul_f32 v[114:115], v[116:117], v[130:131] op_sel_hi:[1,0]
	v_med3_f32 v117, v118, s63, v235
	v_med3_f32 v118, v119, s63, v235
	v_cvt_pk_fp8_f32 v116, v117, v118
	v_med3_f32 v118, v120, s63, v235
	v_med3_f32 v119, v121, s63, v235
	v_med3_f32 v120, v124, s63, v235
	v_med3_f32 v121, v125, s63, v235
	v_cvt_pk_fp8_f32 v117, v120, v121
	v_pk_mul_f32 v[122:123], v[114:115], v[122:123]
	v_cvt_f32_i32_e32 v113, v113
	v_cvt_f32_i32_e32 v112, v112
	v_cvt_pk_fp8_f32 v116, v118, v119 op_sel:[0,0,1]
	v_med3_f32 v118, v122, s63, v235
	v_med3_f32 v119, v123, s63, v235
	v_cvt_pk_fp8_f32 v117, v118, v119 op_sel:[0,0,1]
	v_pk_mul_f32 v[118:119], v[204:205], v[224:225] op_sel_hi:[1,0]
	v_cvt_f32_i32_e32 v111, v111
	v_mul_f32_e32 v120, 0xbfb8aa3b, v118
	v_pk_mul_f32 v[124:125], v[112:113], v[120:121] op_sel_hi:[1,0]
	v_cvt_f32_i32_e32 v110, v110
	v_cvt_f32_i32_e32 v107, v107
	v_cvt_f32_i32_e32 v106, v106
	v_cvt_f32_i32_e32 v103, v103
	v_cvt_f32_i32_e32 v102, v102
	v_cvt_f32_i32_e32 v105, v105
	v_cvt_f32_i32_e32 v104, v104
	v_exp_f32_e32 v124, v124
	v_exp_f32_e32 v125, v125
	v_pk_mul_f32 v[122:123], v[110:111], v[120:121] op_sel_hi:[1,0]
	v_pk_mul_f32 v[104:105], v[104:105], v[112:113]
	v_pk_mul_f32 v[102:103], v[102:103], v[110:111]
	v_pk_add_f32 v[110:111], v[124:125], 1.0 op_sel_hi:[1,0]
	v_pk_mul_f32 v[112:113], v[106:107], v[120:121] op_sel_hi:[1,0]
	v_cvt_f32_i32_e32 v109, v109
	v_cvt_f32_i32_e32 v108, v108
	v_rcp_f32_e32 v110, v110
	v_rcp_f32_e32 v111, v111
	v_exp_f32_e32 v112, v112
	v_exp_f32_e32 v113, v113
	v_mul_f32_e32 v118, v118, v119
	v_mul_f32_e32 v118, 0x41000000, v118
	v_pk_mul_f32 v[104:105], v[104:105], v[118:119] op_sel_hi:[1,0]
	v_exp_f32_e32 v122, v122
	v_exp_f32_e32 v123, v123
	v_pk_mul_f32 v[104:105], v[104:105], v[110:111]
	v_pk_add_f32 v[110:111], v[112:113], 1.0 op_sel_hi:[1,0]
	v_pk_mul_f32 v[112:113], v[108:109], v[120:121] op_sel_hi:[1,0]
	v_cvt_f32_i32_e32 v99, v99
	v_cvt_f32_i32_e32 v98, v98
	v_exp_f32_e32 v112, v112
	v_exp_f32_e32 v113, v113
	v_cvt_f32_i32_e32 v101, v101
	v_cvt_f32_i32_e32 v100, v100
	v_pk_add_f32 v[122:123], v[122:123], 1.0 op_sel_hi:[1,0]
	v_rcp_f32_e32 v110, v110
	v_rcp_f32_e32 v122, v122
	v_rcp_f32_e32 v123, v123
	v_rcp_f32_e32 v111, v111
	v_pk_mul_f32 v[98:99], v[98:99], v[106:107]
	v_pk_add_f32 v[106:107], v[112:113], 1.0 op_sel_hi:[1,0]
	v_pk_mul_f32 v[102:103], v[102:103], v[118:119] op_sel_hi:[1,0]
	v_rcp_f32_e32 v106, v106
	v_rcp_f32_e32 v107, v107
	v_pk_mul_f32 v[100:101], v[100:101], v[108:109]
	v_pk_mul_f32 v[98:99], v[98:99], v[118:119] op_sel_hi:[1,0]
	v_pk_mul_f32 v[102:103], v[102:103], v[122:123]
	v_pk_mul_f32 v[108:109], v[98:99], v[110:111]
	v_pk_mul_f32 v[98:99], v[100:101], v[118:119] op_sel_hi:[1,0]
	v_cvt_f32_i32_e32 v97, v97
	v_pk_mul_f32 v[100:101], v[98:99], v[106:107]
	v_med3_f32 v99, v102, s63, v235
	v_med3_f32 v102, v103, s63, v235
	v_cvt_pk_fp8_f32 v98, v99, v102
	v_med3_f32 v102, v104, s63, v235
	v_med3_f32 v103, v105, s63, v235
	v_med3_f32 v104, v108, s63, v235
	v_med3_f32 v105, v109, s63, v235
	v_cvt_pk_fp8_f32 v99, v104, v105
	v_cvt_f32_i32_e32 v96, v96
	v_med3_f32 v100, v100, s63, v235
	v_med3_f32 v101, v101, s63, v235
	v_cvt_pk_fp8_f32 v99, v100, v101 op_sel:[0,0,1]
	v_pk_mul_f32 v[100:101], v[204:205], v[226:227] op_sel_hi:[1,0]
	v_cvt_pk_fp8_f32 v98, v102, v103 op_sel:[0,0,1]
	v_mul_f32_e32 v102, 0xbfb8aa3b, v100
	v_pk_mul_f32 v[106:107], v[96:97], v[102:103] op_sel_hi:[1,0]
	v_cvt_f32_i32_e32 v95, v95
	v_cvt_f32_i32_e32 v94, v94
	v_cvt_f32_i32_e32 v91, v91
	v_cvt_f32_i32_e32 v90, v90
	v_cvt_f32_i32_e32 v87, v87
	v_cvt_f32_i32_e32 v86, v86
	v_cvt_f32_i32_e32 v89, v89
	v_cvt_f32_i32_e32 v88, v88
	v_exp_f32_e32 v106, v106
	v_exp_f32_e32 v107, v107
	v_pk_mul_f32 v[104:105], v[94:95], v[102:103] op_sel_hi:[1,0]
	v_pk_mul_f32 v[88:89], v[88:89], v[96:97]
	v_pk_mul_f32 v[86:87], v[86:87], v[94:95]
	v_pk_add_f32 v[94:95], v[106:107], 1.0 op_sel_hi:[1,0]
	v_pk_mul_f32 v[96:97], v[90:91], v[102:103] op_sel_hi:[1,0]
	v_cvt_f32_i32_e32 v93, v93
	v_cvt_f32_i32_e32 v92, v92
	v_rcp_f32_e32 v94, v94
	v_rcp_f32_e32 v95, v95
	v_exp_f32_e32 v96, v96
	v_exp_f32_e32 v97, v97
	v_mul_f32_e32 v100, v100, v101
	v_mul_f32_e32 v100, 0x41000000, v100
	v_pk_mul_f32 v[88:89], v[88:89], v[100:101] op_sel_hi:[1,0]
	v_exp_f32_e32 v104, v104
	v_exp_f32_e32 v105, v105
	v_pk_mul_f32 v[88:89], v[88:89], v[94:95]
	v_pk_add_f32 v[94:95], v[96:97], 1.0 op_sel_hi:[1,0]
	v_pk_mul_f32 v[96:97], v[92:93], v[102:103] op_sel_hi:[1,0]
	v_cvt_f32_i32_e32 v83, v83
	v_cvt_f32_i32_e32 v82, v82
	v_exp_f32_e32 v96, v96
	v_exp_f32_e32 v97, v97
	v_cvt_f32_i32_e32 v85, v85
	v_cvt_f32_i32_e32 v84, v84
	v_pk_add_f32 v[104:105], v[104:105], 1.0 op_sel_hi:[1,0]
	v_pk_mul_f32 v[82:83], v[82:83], v[90:91]
	v_rcp_f32_e32 v104, v104
	v_rcp_f32_e32 v105, v105
	v_pk_add_f32 v[90:91], v[96:97], 1.0 op_sel_hi:[1,0]
	v_rcp_f32_e32 v94, v94
	v_rcp_f32_e32 v95, v95
	v_rcp_f32_e32 v90, v90
	v_rcp_f32_e32 v91, v91
	v_pk_mul_f32 v[86:87], v[86:87], v[100:101] op_sel_hi:[1,0]
	v_pk_mul_f32 v[84:85], v[84:85], v[92:93]
	v_pk_mul_f32 v[86:87], v[86:87], v[104:105]
	v_pk_mul_f32 v[82:83], v[82:83], v[100:101] op_sel_hi:[1,0]
	v_pk_mul_f32 v[84:85], v[84:85], v[100:101] op_sel_hi:[1,0]
	v_pk_mul_f32 v[82:83], v[82:83], v[94:95]
	v_pk_mul_f32 v[84:85], v[84:85], v[90:91]
	v_med3_f32 v90, v86, s63, v235
	v_med3_f32 v87, v87, s63, v235
	v_cvt_pk_fp8_f32 v86, v90, v87
	v_med3_f32 v82, v82, s63, v235
	v_med3_f32 v83, v83, s63, v235
	v_cvt_pk_fp8_f32 v87, v82, v83
	v_cvt_f32_i32_e32 v81, v81
	v_cvt_f32_i32_e32 v80, v80
	v_med3_f32 v82, v84, s63, v235
	v_med3_f32 v83, v85, s63, v235
	v_cvt_pk_fp8_f32 v87, v82, v83 op_sel:[0,0,1]
	v_pk_mul_f32 v[82:83], v[204:205], v[228:229] op_sel_hi:[1,0]
	v_cvt_f32_i32_e32 v79, v79
	v_mul_f32_e32 v84, 0xbfb8aa3b, v82
	v_pk_mul_f32 v[90:91], v[80:81], v[84:85] op_sel_hi:[1,0]
	v_cvt_f32_i32_e32 v78, v78
	v_cvt_f32_i32_e32 v75, v75
	v_cvt_f32_i32_e32 v74, v74
	v_cvt_f32_i32_e32 v71, v71
	v_cvt_f32_i32_e32 v70, v70
	v_cvt_f32_i32_e32 v73, v73
	v_cvt_f32_i32_e32 v72, v72
	v_exp_f32_e32 v90, v90
	v_exp_f32_e32 v91, v91
	v_med3_f32 v88, v88, s63, v235
	v_med3_f32 v89, v89, s63, v235
	v_cvt_pk_fp8_f32 v86, v88, v89 op_sel:[0,0,1]
	v_pk_mul_f32 v[88:89], v[78:79], v[84:85] op_sel_hi:[1,0]
	v_pk_mul_f32 v[72:73], v[72:73], v[80:81]
	v_pk_mul_f32 v[70:71], v[70:71], v[78:79]
	v_pk_add_f32 v[78:79], v[90:91], 1.0 op_sel_hi:[1,0]
	v_pk_mul_f32 v[80:81], v[74:75], v[84:85] op_sel_hi:[1,0]
	v_cvt_f32_i32_e32 v77, v77
	v_cvt_f32_i32_e32 v76, v76
	v_rcp_f32_e32 v78, v78
	v_rcp_f32_e32 v79, v79
	v_exp_f32_e32 v80, v80
	v_exp_f32_e32 v81, v81
	v_mul_f32_e32 v82, v82, v83
	v_mul_f32_e32 v82, 0x41000000, v82
	v_pk_mul_f32 v[72:73], v[72:73], v[82:83] op_sel_hi:[1,0]
	v_exp_f32_e32 v88, v88
	v_exp_f32_e32 v89, v89
	v_pk_mul_f32 v[72:73], v[72:73], v[78:79]
	v_pk_add_f32 v[78:79], v[80:81], 1.0 op_sel_hi:[1,0]
	v_pk_mul_f32 v[80:81], v[76:77], v[84:85] op_sel_hi:[1,0]
	v_cvt_f32_i32_e32 v67, v67
	v_cvt_f32_i32_e32 v66, v66
	v_exp_f32_e32 v80, v80
	v_exp_f32_e32 v81, v81
	v_cvt_f32_i32_e32 v69, v69
	v_cvt_f32_i32_e32 v68, v68
	v_pk_add_f32 v[88:89], v[88:89], 1.0 op_sel_hi:[1,0]
	v_pk_mul_f32 v[66:67], v[66:67], v[74:75]
	v_rcp_f32_e32 v88, v88
	v_rcp_f32_e32 v89, v89
	v_pk_add_f32 v[74:75], v[80:81], 1.0 op_sel_hi:[1,0]
	v_rcp_f32_e32 v78, v78
	v_rcp_f32_e32 v79, v79
	v_rcp_f32_e32 v74, v74
	v_rcp_f32_e32 v75, v75
	v_pk_mul_f32 v[70:71], v[70:71], v[82:83] op_sel_hi:[1,0]
	v_pk_mul_f32 v[68:69], v[68:69], v[76:77]
	v_pk_mul_f32 v[70:71], v[70:71], v[88:89]
	v_pk_mul_f32 v[66:67], v[66:67], v[82:83] op_sel_hi:[1,0]
	v_pk_mul_f32 v[68:69], v[68:69], v[82:83] op_sel_hi:[1,0]
	v_pk_mul_f32 v[66:67], v[66:67], v[78:79]
	v_pk_mul_f32 v[68:69], v[68:69], v[74:75]
	v_med3_f32 v74, v70, s63, v235
	v_med3_f32 v71, v71, s63, v235
	v_cvt_pk_fp8_f32 v70, v74, v71
	v_med3_f32 v66, v66, s63, v235
	v_med3_f32 v67, v67, s63, v235
	v_cvt_pk_fp8_f32 v71, v66, v67
	s_lshl_b32 s4, s24, 2
	s_or_b32 s4, s4, s57
	v_cvt_f32_i32_e32 v65, v65
	v_cvt_f32_i32_e32 v64, v64
	s_ashr_i32 s5, s4, 31
	v_med3_f32 v66, v68, s63, v235
	v_med3_f32 v67, v69, s63, v235
	s_lshl_b64 s[4:5], s[4:5], 13
	s_mul_i32 s17, s22, 0x1c0000
	v_cvt_pk_fp8_f32 v71, v66, v67 op_sel:[0,0,1]
	v_pk_mul_f32 v[66:67], v[204:205], v[230:231] op_sel_hi:[1,0]
	s_mul_hi_i32 s15, s22, 0x1c0000
	s_add_u32 s17, s55, s17
	v_med3_f32 v72, v72, s63, v235
	v_med3_f32 v73, v73, s63, v235
	v_mul_f32_e32 v68, 0xbfb8aa3b, v66
	s_addc_u32 s15, s56, s15
	v_cvt_pk_fp8_f32 v70, v72, v73 op_sel:[0,0,1]
	v_pk_mul_f32 v[72:73], v[64:65], v[68:69] op_sel_hi:[1,0]
	s_add_u32 s4, s17, s4
	v_cvt_f32_i32_e32 v63, v63
	v_cvt_f32_i32_e32 v62, v62
	v_cvt_f32_i32_e32 v59, v59
	v_cvt_f32_i32_e32 v58, v58
	v_cvt_f32_i32_e32 v55, v55
	v_cvt_f32_i32_e32 v54, v54
	v_cvt_f32_i32_e32 v57, v57
	v_cvt_f32_i32_e32 v56, v56
	v_exp_f32_e32 v72, v72
	v_exp_f32_e32 v73, v73
	s_addc_u32 s5, s15, s5
	v_lshl_add_u64 v[114:115], s[4:5], 0, v[206:207]
	v_lshl_add_u64 v[114:115], v[114:115], 0, v[194:195]
	global_store_dwordx2 v[114:115], v[116:117], off
	global_store_dwordx2 v[114:115], v[98:99], off offset:512
	global_store_dwordx2 v[114:115], v[86:87], off offset:1024
	global_store_dwordx2 v[114:115], v[70:71], off offset:1536
	v_pk_mul_f32 v[70:71], v[62:63], v[68:69] op_sel_hi:[1,0]
	v_pk_mul_f32 v[56:57], v[56:57], v[64:65]
	v_pk_mul_f32 v[54:55], v[54:55], v[62:63]
	v_pk_add_f32 v[62:63], v[72:73], 1.0 op_sel_hi:[1,0]
	v_pk_mul_f32 v[64:65], v[58:59], v[68:69] op_sel_hi:[1,0]
	v_cvt_f32_i32_e32 v61, v61
	v_cvt_f32_i32_e32 v60, v60
	v_exp_f32_e32 v70, v70
	v_exp_f32_e32 v71, v71
	v_rcp_f32_e32 v62, v62
	v_rcp_f32_e32 v63, v63
	v_exp_f32_e32 v64, v64
	v_exp_f32_e32 v65, v65
	v_mul_f32_e32 v66, v66, v67
	v_mul_f32_e32 v66, 0x41000000, v66
	v_pk_mul_f32 v[56:57], v[56:57], v[66:67] op_sel_hi:[1,0]
	v_cvt_f32_i32_e32 v51, v51
	v_cvt_f32_i32_e32 v50, v50
	v_pk_add_f32 v[70:71], v[70:71], 1.0 op_sel_hi:[1,0]
	v_pk_mul_f32 v[56:57], v[56:57], v[62:63]
	v_pk_add_f32 v[62:63], v[64:65], 1.0 op_sel_hi:[1,0]
	v_pk_mul_f32 v[64:65], v[60:61], v[68:69] op_sel_hi:[1,0]
	v_rcp_f32_e32 v70, v70
	v_rcp_f32_e32 v71, v71
	v_exp_f32_e32 v64, v64
	v_exp_f32_e32 v65, v65
	v_cvt_f32_i32_e32 v53, v53
	v_cvt_f32_i32_e32 v52, v52
	v_rcp_f32_e32 v62, v62
	v_rcp_f32_e32 v63, v63
	v_pk_mul_f32 v[54:55], v[54:55], v[66:67] op_sel_hi:[1,0]
	v_pk_mul_f32 v[50:51], v[50:51], v[58:59]
	v_pk_mul_f32 v[54:55], v[54:55], v[70:71]
	v_pk_add_f32 v[58:59], v[64:65], 1.0 op_sel_hi:[1,0]
	v_pk_mul_f32 v[50:51], v[50:51], v[66:67] op_sel_hi:[1,0]
	v_pk_mul_f32 v[52:53], v[52:53], v[60:61]
	v_rcp_f32_e32 v58, v58
	v_rcp_f32_e32 v59, v59
	v_pk_mul_f32 v[50:51], v[50:51], v[62:63]
	v_med3_f32 v60, v54, s63, v235
	v_med3_f32 v55, v55, s63, v235
	v_cvt_pk_fp8_f32 v54, v60, v55
	v_med3_f32 v50, v50, s63, v235
	v_med3_f32 v51, v51, s63, v235
	v_cvt_pk_fp8_f32 v55, v50, v51
	v_pk_mul_f32 v[52:53], v[52:53], v[66:67] op_sel_hi:[1,0]
	v_cvt_f32_i32_e32 v49, v49
	v_pk_mul_f32 v[52:53], v[52:53], v[58:59]
	v_cvt_f32_i32_e32 v48, v48
	v_med3_f32 v50, v52, s63, v235
	v_med3_f32 v51, v53, s63, v235
	v_cvt_pk_fp8_f32 v55, v50, v51 op_sel:[0,0,1]
	v_pk_mul_f32 v[50:51], v[204:205], v[232:233] op_sel_hi:[1,0]
	v_cvt_f32_i32_e32 v47, v47
	v_mul_f32_e32 v52, 0xbfb8aa3b, v50
	v_pk_mul_f32 v[60:61], v[48:49], v[52:53] op_sel_hi:[1,0]
	v_cvt_f32_i32_e32 v46, v46
	v_cvt_f32_i32_e32 v43, v43
	v_cvt_f32_i32_e32 v42, v42
	v_cvt_f32_i32_e32 v39, v39
	v_cvt_f32_i32_e32 v38, v38
	v_cvt_f32_i32_e32 v41, v41
	v_cvt_f32_i32_e32 v40, v40
	v_exp_f32_e32 v60, v60
	v_exp_f32_e32 v61, v61
	v_med3_f32 v56, v56, s63, v235
	v_med3_f32 v57, v57, s63, v235
	v_cvt_pk_fp8_f32 v54, v56, v57 op_sel:[0,0,1]
	v_pk_mul_f32 v[56:57], v[46:47], v[52:53] op_sel_hi:[1,0]
	v_pk_mul_f32 v[40:41], v[40:41], v[48:49]
	v_pk_mul_f32 v[38:39], v[38:39], v[46:47]
	v_pk_add_f32 v[46:47], v[60:61], 1.0 op_sel_hi:[1,0]
	v_pk_mul_f32 v[48:49], v[42:43], v[52:53] op_sel_hi:[1,0]
	v_cvt_f32_i32_e32 v45, v45
	v_cvt_f32_i32_e32 v44, v44
	v_rcp_f32_e32 v46, v46
	v_rcp_f32_e32 v47, v47
	v_exp_f32_e32 v48, v48
	v_exp_f32_e32 v49, v49
	v_mul_f32_e32 v50, v50, v51
	v_mul_f32_e32 v50, 0x41000000, v50
	v_pk_mul_f32 v[40:41], v[40:41], v[50:51] op_sel_hi:[1,0]
	v_exp_f32_e32 v56, v56
	v_exp_f32_e32 v57, v57
	v_pk_mul_f32 v[40:41], v[40:41], v[46:47]
	v_pk_add_f32 v[46:47], v[48:49], 1.0 op_sel_hi:[1,0]
	v_pk_mul_f32 v[48:49], v[44:45], v[52:53] op_sel_hi:[1,0]
	v_cvt_f32_i32_e32 v35, v35
	v_cvt_f32_i32_e32 v34, v34
	v_exp_f32_e32 v48, v48
	v_exp_f32_e32 v49, v49
	v_cvt_f32_i32_e32 v37, v37
	v_cvt_f32_i32_e32 v36, v36
	v_pk_add_f32 v[56:57], v[56:57], 1.0 op_sel_hi:[1,0]
	v_pk_mul_f32 v[34:35], v[34:35], v[42:43]
	v_rcp_f32_e32 v56, v56
	v_rcp_f32_e32 v57, v57
	v_pk_add_f32 v[42:43], v[48:49], 1.0 op_sel_hi:[1,0]
	v_rcp_f32_e32 v46, v46
	v_rcp_f32_e32 v47, v47
	v_rcp_f32_e32 v42, v42
	v_rcp_f32_e32 v43, v43
	v_pk_mul_f32 v[38:39], v[38:39], v[50:51] op_sel_hi:[1,0]
	v_pk_mul_f32 v[36:37], v[36:37], v[44:45]
	v_pk_mul_f32 v[38:39], v[38:39], v[56:57]
	v_pk_mul_f32 v[34:35], v[34:35], v[50:51] op_sel_hi:[1,0]
	v_pk_mul_f32 v[36:37], v[36:37], v[50:51] op_sel_hi:[1,0]
	v_pk_mul_f32 v[34:35], v[34:35], v[46:47]
	v_pk_mul_f32 v[36:37], v[36:37], v[42:43]
	v_med3_f32 v42, v38, s63, v235
	v_med3_f32 v39, v39, s63, v235
	v_cvt_pk_fp8_f32 v38, v42, v39
	v_med3_f32 v34, v34, s63, v235
	v_med3_f32 v35, v35, s63, v235
	v_cvt_pk_fp8_f32 v39, v34, v35
	v_med3_f32 v40, v40, s63, v235
	v_med3_f32 v41, v41, s63, v235
	v_med3_f32 v34, v36, s63, v235
	v_med3_f32 v35, v37, s63, v235
	v_cvt_pk_fp8_f32 v38, v40, v41 op_sel:[0,0,1]
	v_cvt_pk_fp8_f32 v39, v34, v35 op_sel:[0,0,1]
	v_lshl_add_u64 v[34:35], s[4:5], 0, v[210:211]
	v_cvt_f32_i32_e32 v33, v33
	v_cvt_f32_i32_e32 v32, v32
	v_lshl_add_u64 v[34:35], v[34:35], 0, v[194:195]
	global_store_dwordx2 v[34:35], v[38:39], off
	v_pk_mul_f32 v[34:35], v[204:205], v[234:235] op_sel_hi:[1,0]
	v_cvt_f32_i32_e32 v31, v31
	v_mul_f32_e32 v36, 0xbfb8aa3b, v34
	v_pk_mul_f32 v[40:41], v[32:33], v[36:37] op_sel_hi:[1,0]
	v_cvt_f32_i32_e32 v30, v30
	v_cvt_f32_i32_e32 v27, v27
	v_cvt_f32_i32_e32 v26, v26
	v_cvt_f32_i32_e32 v23, v23
	v_cvt_f32_i32_e32 v22, v22
	v_cvt_f32_i32_e32 v25, v25
	v_cvt_f32_i32_e32 v24, v24
	v_exp_f32_e32 v40, v40
	v_exp_f32_e32 v41, v41
	v_pk_mul_f32 v[38:39], v[30:31], v[36:37] op_sel_hi:[1,0]
	v_pk_mul_f32 v[24:25], v[24:25], v[32:33]
	v_pk_mul_f32 v[22:23], v[22:23], v[30:31]
	v_pk_add_f32 v[30:31], v[40:41], 1.0 op_sel_hi:[1,0]
	v_pk_mul_f32 v[32:33], v[26:27], v[36:37] op_sel_hi:[1,0]
	v_cvt_f32_i32_e32 v29, v29
	v_cvt_f32_i32_e32 v28, v28
	v_exp_f32_e32 v38, v38
	v_exp_f32_e32 v39, v39
	v_rcp_f32_e32 v30, v30
	v_rcp_f32_e32 v31, v31
	v_exp_f32_e32 v32, v32
	v_exp_f32_e32 v33, v33
	v_mul_f32_e32 v34, v34, v35
	v_mul_f32_e32 v34, 0x41000000, v34
	v_pk_mul_f32 v[24:25], v[24:25], v[34:35] op_sel_hi:[1,0]
	v_cvt_f32_i32_e32 v19, v19
	v_cvt_f32_i32_e32 v18, v18
	v_pk_add_f32 v[38:39], v[38:39], 1.0 op_sel_hi:[1,0]
	v_pk_mul_f32 v[24:25], v[24:25], v[30:31]
	v_pk_add_f32 v[30:31], v[32:33], 1.0 op_sel_hi:[1,0]
	v_pk_mul_f32 v[32:33], v[28:29], v[36:37] op_sel_hi:[1,0]
	v_rcp_f32_e32 v38, v38
	v_rcp_f32_e32 v39, v39
	v_exp_f32_e32 v32, v32
	v_exp_f32_e32 v33, v33
	v_cvt_f32_i32_e32 v21, v21
	v_cvt_f32_i32_e32 v20, v20
	v_rcp_f32_e32 v30, v30
	v_rcp_f32_e32 v31, v31
	v_pk_mul_f32 v[22:23], v[22:23], v[34:35] op_sel_hi:[1,0]
	v_pk_mul_f32 v[18:19], v[18:19], v[26:27]
	v_pk_mul_f32 v[22:23], v[22:23], v[38:39]
	v_pk_add_f32 v[26:27], v[32:33], 1.0 op_sel_hi:[1,0]
	v_pk_mul_f32 v[18:19], v[18:19], v[34:35] op_sel_hi:[1,0]
	v_pk_mul_f32 v[20:21], v[20:21], v[28:29]
	v_rcp_f32_e32 v26, v26
	v_rcp_f32_e32 v27, v27
	v_pk_mul_f32 v[18:19], v[18:19], v[30:31]
	v_med3_f32 v28, v22, s63, v235
	v_med3_f32 v23, v23, s63, v235
	v_cvt_pk_fp8_f32 v22, v28, v23
	v_med3_f32 v18, v18, s63, v235
	v_med3_f32 v19, v19, s63, v235
	v_cvt_pk_fp8_f32 v23, v18, v19
	v_pk_mul_f32 v[20:21], v[20:21], v[34:35] op_sel_hi:[1,0]
	v_cvt_f32_i32_e32 v17, v17
	v_pk_mul_f32 v[20:21], v[20:21], v[26:27]
	v_cvt_f32_i32_e32 v16, v16
	v_med3_f32 v18, v20, s63, v235
	v_med3_f32 v19, v21, s63, v235
	v_cvt_pk_fp8_f32 v23, v18, v19 op_sel:[0,0,1]
	v_pk_mul_f32 v[18:19], v[204:205], v[236:237] op_sel_hi:[1,0]
	v_cvt_f32_i32_e32 v15, v15
	v_mul_f32_e32 v20, 0xbfb8aa3b, v18
	v_pk_mul_f32 v[28:29], v[16:17], v[20:21] op_sel_hi:[1,0]
	v_cvt_f32_i32_e32 v14, v14
	v_cvt_f32_i32_e32 v11, v11
	v_cvt_f32_i32_e32 v10, v10
	v_cvt_f32_i32_e32 v7, v7
	v_cvt_f32_i32_e32 v6, v6
	v_cvt_f32_i32_e32 v9, v9
	v_cvt_f32_i32_e32 v8, v8
	v_exp_f32_e32 v28, v28
	v_exp_f32_e32 v29, v29
	v_med3_f32 v24, v24, s63, v235
	v_med3_f32 v25, v25, s63, v235
	v_cvt_pk_fp8_f32 v22, v24, v25 op_sel:[0,0,1]
	v_pk_mul_f32 v[24:25], v[14:15], v[20:21] op_sel_hi:[1,0]
	v_pk_mul_f32 v[8:9], v[8:9], v[16:17]
	v_pk_mul_f32 v[6:7], v[6:7], v[14:15]
	v_pk_add_f32 v[14:15], v[28:29], 1.0 op_sel_hi:[1,0]
	v_pk_mul_f32 v[16:17], v[10:11], v[20:21] op_sel_hi:[1,0]
	v_cvt_f32_i32_e32 v13, v13
	v_cvt_f32_i32_e32 v12, v12
	v_rcp_f32_e32 v14, v14
	v_rcp_f32_e32 v15, v15
	v_exp_f32_e32 v16, v16
	v_exp_f32_e32 v17, v17
	v_mul_f32_e32 v18, v18, v19
	v_mul_f32_e32 v18, 0x41000000, v18
	v_pk_mul_f32 v[8:9], v[8:9], v[18:19] op_sel_hi:[1,0]
	v_exp_f32_e32 v24, v24
	v_exp_f32_e32 v25, v25
	v_pk_mul_f32 v[8:9], v[8:9], v[14:15]
	v_pk_add_f32 v[14:15], v[16:17], 1.0 op_sel_hi:[1,0]
	v_pk_mul_f32 v[16:17], v[12:13], v[20:21] op_sel_hi:[1,0]
	v_cvt_f32_i32_e32 v3, v3
	v_cvt_f32_i32_e32 v2, v2
	v_exp_f32_e32 v16, v16
	v_exp_f32_e32 v17, v17
	v_cvt_f32_i32_e32 v5, v5
	v_cvt_f32_i32_e32 v4, v4
	v_pk_add_f32 v[24:25], v[24:25], 1.0 op_sel_hi:[1,0]
	v_pk_mul_f32 v[2:3], v[2:3], v[10:11]
	v_rcp_f32_e32 v24, v24
	v_rcp_f32_e32 v25, v25
	v_pk_add_f32 v[10:11], v[16:17], 1.0 op_sel_hi:[1,0]
	v_rcp_f32_e32 v14, v14
	v_rcp_f32_e32 v15, v15
	v_rcp_f32_e32 v10, v10
	v_rcp_f32_e32 v11, v11
	v_pk_mul_f32 v[6:7], v[6:7], v[18:19] op_sel_hi:[1,0]
	v_pk_mul_f32 v[4:5], v[4:5], v[12:13]
	v_pk_mul_f32 v[6:7], v[6:7], v[24:25]
	v_pk_mul_f32 v[2:3], v[2:3], v[18:19] op_sel_hi:[1,0]
	v_pk_mul_f32 v[4:5], v[4:5], v[18:19] op_sel_hi:[1,0]
	v_pk_mul_f32 v[2:3], v[2:3], v[14:15]
	v_pk_mul_f32 v[4:5], v[4:5], v[10:11]
	v_med3_f32 v10, v6, s63, v235
	v_med3_f32 v7, v7, s63, v235
	v_cvt_pk_fp8_f32 v6, v10, v7
	v_med3_f32 v2, v2, s63, v235
	v_med3_f32 v3, v3, s63, v235
	v_cvt_pk_fp8_f32 v7, v2, v3
	v_med3_f32 v8, v8, s63, v235
	v_med3_f32 v9, v9, s63, v235
	v_med3_f32 v2, v4, s63, v235
	v_med3_f32 v3, v5, s63, v235
	v_cvt_pk_fp8_f32 v6, v8, v9 op_sel:[0,0,1]
	v_cvt_pk_fp8_f32 v7, v2, v3 op_sel:[0,0,1]
	v_lshl_add_u64 v[58:59], s[4:5], 0, v[208:209]
	v_lshl_add_u64 v[26:27], s[4:5], 0, v[212:213]
	v_lshl_add_u64 v[2:3], s[4:5], 0, v[214:215]
	v_lshl_add_u64 v[58:59], v[58:59], 0, v[194:195]
	v_lshl_add_u64 v[26:27], v[26:27], 0, v[194:195]
	v_lshl_add_u64 v[2:3], v[2:3], 0, v[194:195]
	s_and_b64 vcc, exec, s[0:1]
	s_mov_b64 s[0:1], -1
	global_store_dwordx2 v[58:59], v[54:55], off
	global_store_dwordx2 v[26:27], v[22:23], off
	global_store_dwordx2 v[2:3], v[6:7], off
	s_cbranch_vccnz .LBB0_3824
	s_andn2_b64 vcc, exec, s[8:9]
	s_cbranch_vccnz .LBB0_3823
	s_barrier
	s_branch .LBB0_3823
